# deferred weight-conversion split: 2600 gate/up + 1300 down tiles deferred, idle-slot quotas 6/8/7/8
# speedup vs baseline: 1.0036x; 1.0036x over previous
; __device__ __forceinline__ void bt_load(const float* __restrict__ src, int N, int perm, int it, int ntn, f32x4 (&v)[8]) {
;     const int wid = threadIdx.x >> 6, lane = threadIdx.x & 63;
;     const int per = 16 * ntn, z = it / per, r = it % per, kt = r / ntn, nt = r % ntn;
;     const int np = nt * 256 + lane * 4;
;     const int sc = perm ? (nt * 128 + (lane & 31) * 4 + (lane >> 5) * 1024) : np;
;     const float* p = src + (size_t)z * 1024 * N + (size_t)(kt * 64 + wid * 8) * N + sc;
; #pragma unroll
;     for (int i = 0; i < 8; ++i) v[i] = __builtin_nontemporal_load((const f32x4*)(p + (size_t)i * N));
; }
; __device__ __forceinline__ void ph_big_transpose(const float* __restrict__ src, int N, int perm, int batch, bf16* __restrict__ dst, float* tile  , int G, int ndefer) {
;     const int tid = threadIdx.x, wid = tid >> 6, lane = tid & 63, ntn = N / 256, total = batch * 16 * ntn - ndefer;
;     int it = (int)blockIdx.x;
;     if (it >= total) return;
;     f32x4 cur[8], nxt[8], nx2[8];
;     bt_load(src, N, perm, it, ntn, cur);
;     if (it + G < total) bt_load(src, N, perm, it + G, ntn, nxt);
;     for (; it < total; it += G) {
;         const bool more = it + G < total, more2 = it + 2 * G < total;
;         if (more2) bt_load(src, N, perm, it + 2 * G, ntn, nx2);
.LBB0_63:
	s_cmpk_gt_i32 s2, 0x15d7
	s_waitcnt lgkmcnt(0)
	s_barrier
	s_cbranch_scc1 .LBB0_71
	s_ashr_i32 s0, s2, 31
	s_lshr_b32 s0, s0, 25
	s_add_i32 s1, s2, s0
	s_ashr_i32 s0, s1, 7
	s_and_b32 s1, s1, 0xff80
	s_sub_i32 s1, s2, s1
	s_bfe_i32 s4, s1, 0x80000
	s_bfe_u32 s4, s4, 0x3000c
	s_add_i32 s4, s1, s4
	s_bfe_i32 s5, s4, 0x80000
	s_and_b32 s4, s4, 0xf8
	v_lshlrev_b32_e32 v2, 2, v0
	s_sub_i32 s1, s1, s4
	v_and_b32_e32 v2, 0x7c, v2
	v_lshlrev_b32_e32 v3, 5, v0
	s_movk_i32 s4, 0x400
	s_sext_i32_i8 s1, s1
	v_and_or_b32 v99, v3, s4, v2
	v_lshl_add_u32 v2, s1, 7, v99
	s_ashr_i32 s1, s0, 31
	s_lshl_b64 s[0:1], s[0:1], 23
	s_sext_i32_i16 s5, s5
	s_add_u32 s0, s68, s0
	s_addc_u32 s1, s69, s1
	s_lshl_b32 s4, s5, 3
	v_lshrrev_b32_e32 v3, 3, v0
	s_andn2_b32 s4, s4, 63
	v_and_b32_e32 v110, 56, v3
	v_or_b32_e32 v4, s4, v110
	v_ashrrev_i32_e32 v5, 31, v4
	v_lshlrev_b64 v[4:5], 13, v[4:5]
	v_lshl_add_u64 v[4:5], s[0:1], 0, v[4:5]
	v_ashrrev_i32_e32 v3, 31, v2
	v_lshl_add_u64 v[2:3], v[2:3], 2, v[4:5]
	s_movk_i32 s0, 0x2000
	v_add_co_u32_e32 v4, vcc, s0, v2
	s_movk_i32 s1, 0x4000
	s_nop 0
	v_addc_co_u32_e32 v5, vcc, 0, v3, vcc
	global_load_dwordx4 v[38:41], v[2:3], off nt
	global_load_dwordx4 v[34:37], v[4:5], off nt
	v_add_co_u32_e32 v4, vcc, s1, v2
	s_movk_i32 s4, 0x6000
	s_nop 0
	v_addc_co_u32_e32 v5, vcc, 0, v3, vcc
	v_add_co_u32_e32 v6, vcc, s4, v2
	s_mov_b32 s5, 0x8000
	s_nop 0
	v_addc_co_u32_e32 v7, vcc, 0, v3, vcc
	global_load_dwordx4 v[46:49], v[4:5], off nt
	global_load_dwordx4 v[42:45], v[6:7], off nt
	v_add_co_u32_e32 v4, vcc, s5, v2
	s_mov_b32 s6, 0xa000
	s_nop 0
	v_addc_co_u32_e32 v5, vcc, 0, v3, vcc
	v_add_co_u32_e32 v6, vcc, s6, v2
	s_add_i32 s6, s62, s2
	s_nop 0
	v_addc_co_u32_e32 v7, vcc, 0, v3, vcc
	global_load_dwordx4 v[54:57], v[4:5], off nt
	global_load_dwordx4 v[50:53], v[6:7], off nt
	v_add_co_u32_e32 v4, vcc, 0xc000, v2
	s_cmpk_gt_i32 s6, 0x15d7
	s_nop 0
	v_addc_co_u32_e32 v5, vcc, 0, v3, vcc
	v_add_co_u32_e32 v2, vcc, 0xe000, v2
	s_nop 1
	v_addc_co_u32_e32 v3, vcc, 0, v3, vcc
	global_load_dwordx4 v[62:65], v[4:5], off nt
	global_load_dwordx4 v[58:61], v[2:3], off nt
	s_cbranch_scc1 .LBB0_66
	s_ashr_i32 s7, s6, 31
	s_lshr_b32 s7, s7, 25
	s_add_i32 s7, s6, s7
	s_ashr_i32 s8, s7, 7
	s_and_b32 s7, s7, 0xff80
	s_sub_i32 s6, s6, s7
	s_bfe_i32 s7, s6, 0x80000
	s_bfe_u32 s7, s7, 0x3000c
	s_add_i32 s7, s6, s7
	s_bfe_i32 s9, s7, 0x80000
	s_and_b32 s7, s7, 0xf8
	s_sub_i32 s6, s6, s7
	s_sext_i32_i16 s10, s9
	s_sext_i32_i8 s6, s6
	s_ashr_i32 s9, s8, 31
	v_lshl_add_u32 v2, s6, 7, v99
	s_lshl_b64 s[6:7], s[8:9], 23
	s_add_u32 s6, s68, s6
	s_addc_u32 s7, s69, s7
	s_lshl_b32 s8, s10, 3
	s_andn2_b32 s8, s8, 63
	v_or_b32_e32 v4, s8, v110
	v_ashrrev_i32_e32 v5, 31, v4
	v_lshlrev_b64 v[4:5], 13, v[4:5]
	v_lshl_add_u64 v[4:5], s[6:7], 0, v[4:5]
	v_ashrrev_i32_e32 v3, 31, v2
	v_lshl_add_u64 v[26:27], v[2:3], 2, v[4:5]
	v_add_co_u32_e32 v6, vcc, s0, v26
	s_nop 1
	v_addc_co_u32_e32 v7, vcc, 0, v27, vcc
	v_add_co_u32_e32 v10, vcc, s1, v26
	global_load_dwordx4 v[2:5], v[26:27], off nt
	s_nop 0
	global_load_dwordx4 v[6:9], v[6:7], off nt
	v_addc_co_u32_e32 v11, vcc, 0, v27, vcc
	v_add_co_u32_e32 v14, vcc, s4, v26
	s_nop 1
	v_addc_co_u32_e32 v15, vcc, 0, v27, vcc
	v_add_co_u32_e32 v18, vcc, s5, v26
	global_load_dwordx4 v[10:13], v[10:11], off nt
	s_nop 0
	global_load_dwordx4 v[14:17], v[14:15], off nt
	v_addc_co_u32_e32 v19, vcc, 0, v27, vcc
	v_add_co_u32_e32 v22, vcc, 0xa000, v26
	s_nop 1
	v_addc_co_u32_e32 v23, vcc, 0, v27, vcc
	v_add_co_u32_e32 v28, vcc, 0xc000, v26
	global_load_dwordx4 v[18:21], v[18:19], off nt
	s_nop 0
	global_load_dwordx4 v[22:25], v[22:23], off nt
	v_addc_co_u32_e32 v29, vcc, 0, v27, vcc
	v_add_co_u32_e32 v30, vcc, 0xe000, v26
	s_nop 1
	v_addc_co_u32_e32 v31, vcc, 0, v27, vcc
	global_load_dwordx4 v[26:29], v[28:29], off nt
	s_nop 0
	global_load_dwordx4 v[30:33], v[30:31], off nt

; __device__ __forceinline__ unsigned g8_cvt_pk(float lo, float hi) { unsigned r; asm volatile("v_cvt_pk_bf16_f32 %0, %1, %2" : "=v"(r) : "v"(lo), "v"(hi)); return r; }
; __device__ __forceinline__ void ph_big_transpose(const float* __restrict__ src, int N, int perm, int batch, bf16* __restrict__ dst, float* tile  , int G, int ndefer) {
;     ...
;     for (; it < total; it += G) {
;         const bool more = it + G < total, more2 = it + 2 * G < total;
;         if (more2) bt_load(src, N, perm, it + 2 * G, ntn, nx2);
;         __syncthreads();
; #pragma unroll
;         for (int i = 0; i < 8; ++i) { float* t = tile + (wid * 8 + i) * 257 + lane * 4; t[0] = cur[i][0]; t[1] = cur[i][1]; t[2] = cur[i][2]; t[3] = cur[i][3]; }
;         __syncthreads();
;         const int per = 16 * ntn, z = it / per, r = it % per, kt = r / ntn, nt = r % ntn;
;         bf16* d = dst + (size_t)z * N * 1024 + (((size_t)nt * 16 + kt) << 14);
;         const int kc = lane & 7;
; #pragma unroll
;         for (int pss = 0; pss < 4; ++pss) {
;             const int n = wid * 32 + pss * 8 + (lane >> 3); float f[8];
; #pragma unroll
;             for (int j = 0; j < 8; ++j) f[j] = tile[(kc * 8 + j) * 257 + n];
;             u32x4 w; w.x = g8_cvt_pk(f[0], f[1]); w.y = g8_cvt_pk(f[2], f[3]); w.z = g8_cvt_pk(f[4], f[5]); w.w = g8_cvt_pk(f[6], f[7]);
;             __builtin_nontemporal_store(w, (u32x4*)(d + n * 64 + kc * 8));
;         }
;         if (more) {
; #pragma unroll
;             for (int i = 0; i < 8; ++i) { cur[i] = nxt[i]; nxt[i] = nx2[i]; } }
.LBB0_67:
	s_barrier
	s_waitcnt vmcnt(7)
	ds_write_b128 v111, v[38:41]
	v_add_u32_e32 v38, 0x404, v111
	s_ashr_i32 s9, s8, 31
	s_waitcnt vmcnt(6)
	ds_write2_b32 v38, v34, v35 offset1:1
	v_add_u32_e32 v34, 0x40c, v111
	s_lshr_b32 s9, s9, 25
	ds_write2_b32 v34, v36, v37 offset1:1
	v_add_u32_e32 v34, 0x808, v111
	s_add_i32 s9, s8, s9
	s_waitcnt vmcnt(5)
	ds_write2_b64 v34, v[46:47], v[48:49] offset1:1
	v_add_u32_e32 v34, 0xc0c, v111
	s_ashr_i32 s10, s9, 7
	s_and_b32 s9, s9, 0xff80
	s_waitcnt vmcnt(4)
	ds_write2_b32 v34, v42, v43 offset1:1
	v_add_u32_e32 v34, 0xc14, v111
	s_sub_i32 s9, s8, s9
	s_add_i32 s31, s8, s62
	ds_write2_b32 v34, v44, v45 offset1:1
	s_waitcnt vmcnt(3)
	ds_write_b128 v111, v[54:57] offset:4112
	v_add_u32_e32 v34, 0x1414, v111
	s_bfe_i32 s8, s9, 0x80000
	s_waitcnt vmcnt(2)
	ds_write2_b32 v34, v50, v51 offset1:1
	v_add_u32_e32 v34, 0x141c, v111
	s_bfe_u32 s8, s8, 0x3000c
	ds_write2_b32 v34, v52, v53 offset1:1
	v_add_u32_e32 v34, 0x1818, v111
	s_add_i32 s11, s9, s8
	s_waitcnt vmcnt(1)
	ds_write2_b64 v34, v[62:63], v[64:65] offset1:1
	v_add_u32_e32 v34, 0x1c1c, v111
	s_bfe_i32 s8, s11, 0x80000
	s_and_b32 s11, s11, 0xf8
	s_waitcnt vmcnt(0)
	ds_write2_b32 v34, v58, v59 offset1:1
	v_add_u32_e32 v34, 0x1c24, v111
	s_sext_i32_i16 s8, s8
	s_sub_i32 s30, s9, s11
	s_ashr_i32 s11, s10, 31
	ds_write2_b32 v34, v60, v61 offset1:1
	s_waitcnt lgkmcnt(0)
	s_barrier
	s_lshr_b32 s8, s8, 3
	s_lshl_b64 s[10:11], s[10:11], 22
	ds_read_b32 v34, v112 offset:1028
	ds_read_b32 v35, v112 offset:3084
	ds_read_b32 v36, v112 offset:5140
	ds_read_b32 v37, v112 offset:7196
	ds_read_b32 v38, v112 offset:6168
	ds_read_b32 v39, v112 offset:4112
	ds_read_b32 v40, v112 offset:2056
	ds_read_b32 v41, v112
	s_add_u32 s33, s5, s10
	s_addc_u32 s34, s6, s11
	s_bfe_i64 s[10:11], s[30:31], 0x80000
	s_bfe_i64 s[8:9], s[8:9], 0x100000
	s_lshl_b64 s[10:11], s[10:11], 19
	s_add_u32 s10, s33, s10
	s_addc_u32 s11, s34, s11
	s_lshl_b64 s[8:9], s[8:9], 15
	s_waitcnt lgkmcnt(0)
	v_cvt_pk_bf16_f32 v34, v41, v34
	v_cvt_pk_bf16_f32 v35, v40, v35
	v_cvt_pk_bf16_f32 v36, v39, v36
	v_cvt_pk_bf16_f32 v37, v38, v37
	ds_read_b32 v42, v112 offset:1060
	ds_read_b32 v43, v112 offset:3116
	ds_read_b32 v44, v112 offset:5172
	ds_read_b32 v45, v112 offset:7228
	ds_read_b32 v46, v112 offset:6200
	ds_read_b32 v47, v112 offset:4144
	ds_read_b32 v48, v112 offset:2088
	ds_read_b32 v49, v112 offset:32
	s_add_u32 s8, s10, s8
	s_addc_u32 s9, s11, s9
	v_lshl_add_u64 v[38:39], s[8:9], 0, v[100:101]
	v_mov_b32_e32 v103, v101
	v_lshl_add_u64 v[40:41], v[38:39], 0, v[102:103]
	global_store_dwordx4 v[40:41], v[34:37], off nt
	v_mov_b32_e32 v105, v101
	v_lshl_add_u64 v[40:41], v[38:39], 0, v[104:105]
	s_waitcnt lgkmcnt(0)
	v_cvt_pk_bf16_f32 v34, v49, v42
	v_cvt_pk_bf16_f32 v35, v48, v43
	v_cvt_pk_bf16_f32 v36, v47, v44
	v_cvt_pk_bf16_f32 v37, v46, v45
	ds_read_b32 v42, v112 offset:1092
	ds_read_b32 v43, v112 offset:3148
	ds_read_b32 v44, v112 offset:5204
	ds_read_b32 v45, v112 offset:6232
	ds_read_b32 v46, v112 offset:4176
	ds_read_b32 v47, v112 offset:2120
	ds_read_b32 v48, v112 offset:64
	ds_read_b32 v49, v112 offset:7260
	global_store_dwordx4 v[40:41], v[34:37], off nt
	v_mov_b32_e32 v107, v101
	v_lshl_add_u64 v[40:41], v[38:39], 0, v[106:107]
	s_waitcnt lgkmcnt(1)
	v_cvt_pk_bf16_f32 v34, v48, v42
	v_cvt_pk_bf16_f32 v35, v47, v43
	v_cvt_pk_bf16_f32 v36, v46, v44
	s_waitcnt lgkmcnt(0)
	v_cvt_pk_bf16_f32 v37, v45, v49
	ds_read_b32 v42, v112 offset:1124
	ds_read_b32 v43, v112 offset:3180
	ds_read_b32 v44, v112 offset:5236
	ds_read_b32 v45, v112 offset:6264
	ds_read_b32 v46, v112 offset:4208
	ds_read_b32 v47, v112 offset:2152
	ds_read_b32 v48, v112 offset:96
	ds_read_b32 v49, v112 offset:7292
	v_mov_b32_e32 v109, v101
	global_store_dwordx4 v[40:41], v[34:37], off nt
	v_lshl_add_u64 v[38:39], v[38:39], 0, v[108:109]
	v_mov_b64_e32 v[60:61], v[32:33]
	s_waitcnt lgkmcnt(1)
	v_cvt_pk_bf16_f32 v34, v48, v42
	v_cvt_pk_bf16_f32 v35, v47, v43
	v_cvt_pk_bf16_f32 v36, v46, v44
	s_waitcnt lgkmcnt(0)
	v_cvt_pk_bf16_f32 v37, v45, v49
	global_store_dwordx4 v[38:39], v[34:37], off nt
	v_mov_b64_e32 v[64:65], v[28:29]
	v_mov_b64_e32 v[52:53], v[24:25]
	v_mov_b64_e32 v[56:57], v[20:21]
	v_mov_b64_e32 v[44:45], v[16:17]
	v_mov_b64_e32 v[48:49], v[12:13]
	v_mov_b64_e32 v[36:37], v[8:9]
	v_mov_b64_e32 v[40:41], v[4:5]
	v_mov_b64_e32 v[58:59], v[30:31]
	v_mov_b64_e32 v[62:63], v[26:27]
	v_mov_b64_e32 v[50:51], v[22:23]
	v_mov_b64_e32 v[54:55], v[18:19]
	v_mov_b64_e32 v[42:43], v[14:15]
	v_mov_b64_e32 v[46:47], v[10:11]
	v_mov_b64_e32 v[34:35], v[6:7]
	v_mov_b64_e32 v[38:39], v[2:3]
	v_mov_b64_e32 v[30:31], v[94:95]
	v_mov_b64_e32 v[26:27], v[90:91]
	v_mov_b64_e32 v[22:23], v[86:87]
	v_mov_b64_e32 v[18:19], v[82:83]
	v_mov_b64_e32 v[14:15], v[78:79]
	v_mov_b64_e32 v[10:11], v[74:75]
	v_mov_b64_e32 v[6:7], v[70:71]
	v_mov_b64_e32 v[2:3], v[66:67]
	s_cmpk_lt_i32 s31, 0x15d8
	v_mov_b64_e32 v[32:33], v[96:97]
	v_mov_b64_e32 v[28:29], v[92:93]
	v_mov_b64_e32 v[24:25], v[88:89]
	v_mov_b64_e32 v[20:21], v[84:85]
	v_mov_b64_e32 v[16:17], v[80:81]
	v_mov_b64_e32 v[12:13], v[76:77]
	v_mov_b64_e32 v[8:9], v[72:73]
	v_mov_b64_e32 v[4:5], v[68:69]
	s_mov_b32 s8, s31
	s_cbranch_scc0 .LBB0_70
; __device__ __forceinline__ void bt_load(const float* __restrict__ src, int N, int perm, int it, int ntn, f32x4 (&v)[8]) {
;     const int wid = threadIdx.x >> 6, lane = threadIdx.x & 63;
;     const int per = 16 * ntn, z = it / per, r = it % per, kt = r / ntn, nt = r % ntn;
;     const int np = nt * 256 + lane * 4;
;     const int sc = perm ? (nt * 128 + (lane & 31) * 4 + (lane >> 5) * 1024) : np;
;     const float* p = src + (size_t)z * 1024 * N + (size_t)(kt * 64 + wid * 8) * N + sc;
; #pragma unroll
;     for (int i = 0; i < 8; ++i) v[i] = __builtin_nontemporal_load((const f32x4*)(p + (size_t)i * N));
; }
; __device__ __forceinline__ void ph_big_transpose(const float* __restrict__ src, int N, int perm, int batch, bf16* __restrict__ dst, float* tile  , int G, int ndefer) {
;     ...
;         const bool more = it + G < total, more2 = it + 2 * G < total;
;         if (more2) bt_load(src, N, perm, it + 2 * G, ntn, nx2);
.LBB0_68:
	s_add_i32 s9, s7, s8
	s_cmpk_gt_i32 s9, 0x15d7
	s_cbranch_scc1 .LBB0_67
	s_ashr_i32 s10, s9, 31
	s_lshr_b32 s10, s10, 25
	s_add_i32 s11, s9, s10
	s_ashr_i32 s10, s11, 7
	s_and_b32 s11, s11, 0xff80
	s_sub_i32 s9, s9, s11
	s_bfe_i32 s11, s9, 0x80000
	s_bfe_u32 s11, s11, 0x3000c
	s_add_i32 s11, s9, s11
	s_bfe_i32 s30, s11, 0x80000
	s_and_b32 s11, s11, 0xf8
	s_sub_i32 s9, s9, s11
	s_ashr_i32 s11, s10, 31
	s_lshl_b64 s[10:11], s[10:11], 23
	s_sext_i32_i16 s30, s30
	s_sext_i32_i8 s9, s9
	s_add_u32 s10, s68, s10
	v_lshl_add_u32 v66, s9, 7, v99
	s_addc_u32 s11, s69, s11
	s_lshl_b32 s9, s30, 3
	s_andn2_b32 s9, s9, 63
	v_or_b32_e32 v68, s9, v110
	v_ashrrev_i32_e32 v69, 31, v68
	v_lshlrev_b64 v[68:69], 13, v[68:69]
	v_lshl_add_u64 v[68:69], s[10:11], 0, v[68:69]
	v_ashrrev_i32_e32 v67, 31, v66
	v_lshl_add_u64 v[90:91], v[66:67], 2, v[68:69]
	v_add_co_u32_e32 v70, vcc, s0, v90
	s_nop 1
	v_addc_co_u32_e32 v71, vcc, 0, v91, vcc
	v_add_co_u32_e32 v74, vcc, s1, v90
	global_load_dwordx4 v[66:69], v[90:91], off nt
	s_nop 0
	global_load_dwordx4 v[70:73], v[70:71], off nt
	v_addc_co_u32_e32 v75, vcc, 0, v91, vcc
	v_add_co_u32_e32 v78, vcc, s4, v90
	s_nop 1
	v_addc_co_u32_e32 v79, vcc, 0, v91, vcc
	v_add_co_u32_e32 v82, vcc, 0x8000, v90
	global_load_dwordx4 v[74:77], v[74:75], off nt
	s_nop 0
	global_load_dwordx4 v[78:81], v[78:79], off nt
	v_addc_co_u32_e32 v83, vcc, 0, v91, vcc
	v_add_co_u32_e32 v86, vcc, 0xa000, v90
	s_nop 1
	v_addc_co_u32_e32 v87, vcc, 0, v91, vcc
	v_add_co_u32_e32 v92, vcc, 0xc000, v90
	global_load_dwordx4 v[82:85], v[82:83], off nt
	s_nop 0
	global_load_dwordx4 v[86:89], v[86:87], off nt
	v_addc_co_u32_e32 v93, vcc, 0, v91, vcc
	v_add_co_u32_e32 v94, vcc, 0xe000, v90
	s_nop 1
	v_addc_co_u32_e32 v95, vcc, 0, v91, vcc
	global_load_dwordx4 v[90:93], v[92:93], off nt
	s_nop 0
	global_load_dwordx4 v[94:97], v[94:95], off nt
	s_branch .LBB0_67

; __device__ __forceinline__ void bt_load(const float* __restrict__ src, int N, int perm, int it, int ntn, f32x4 (&v)[8]) {
;     const int wid = threadIdx.x >> 6, lane = threadIdx.x & 63;
;     const int per = 16 * ntn, z = it / per, r = it % per, kt = r / ntn, nt = r % ntn;
;     const int np = nt * 256 + lane * 4;
;     const int sc = perm ? (nt * 128 + (lane & 31) * 4 + (lane >> 5) * 1024) : np;
;     const float* p = src + (size_t)z * 1024 * N + (size_t)(kt * 64 + wid * 8) * N + sc;
; #pragma unroll
;     for (int i = 0; i < 8; ++i) v[i] = __builtin_nontemporal_load((const f32x4*)(p + (size_t)i * N));
; }
; __device__ __forceinline__ void ph_big_transpose(const float* __restrict__ src, int N, int perm, int batch, bf16* __restrict__ dst, float* tile  , int G, int ndefer) {
;     const int tid = threadIdx.x, wid = tid >> 6, lane = tid & 63, ntn = N / 256, total = batch * 16 * ntn - ndefer;
;     int it = (int)blockIdx.x;
;     if (it >= total) return;
;     f32x4 cur[8], nxt[8], nx2[8];
;     bt_load(src, N, perm, it, ntn, cur);
;     if (it + G < total) bt_load(src, N, perm, it + G, ntn, nxt);
;     for (; it < total; it += G) {
;         const bool more = it + G < total, more2 = it + 2 * G < total;
;         if (more2) bt_load(src, N, perm, it + 2 * G, ntn, nx2);
.LBB0_71:
	s_cmpk_gt_i32 s2, 0xaeb
	s_cbranch_scc1 .LBB0_79
	s_ashr_i32 s0, s2, 31
	s_lshr_b32 s0, s0, 26
	s_add_i32 s1, s2, s0
	s_ashr_i32 s0, s1, 6
	s_and_b32 s1, s1, 0xffc0
	s_sub_i32 s1, s2, s1
	s_bfe_i32 s4, s1, 0x80000
	s_bfe_u32 s4, s4, 0x2000d
	s_add_i32 s4, s1, s4
	s_bfe_i32 s5, s4, 0x80000
	s_and_b32 s4, s4, 0xfc
	s_sub_i32 s1, s1, s4
	v_lshlrev_b32_e32 v2, 2, v0
	s_sext_i32_i8 s1, s1
	v_and_b32_e32 v99, 0xfc, v2
	v_lshl_or_b32 v2, s1, 8, v99
	s_ashr_i32 s1, s0, 31
	s_lshl_b64 s[0:1], s[0:1], 22
	s_sext_i32_i16 s5, s5
	s_add_u32 s0, s72, s0
	s_addc_u32 s1, s73, s1
	s_lshl_b32 s4, s5, 4
	v_lshrrev_b32_e32 v3, 3, v0
	s_andn2_b32 s4, s4, 63
	v_and_b32_e32 v110, 56, v3
	v_or_b32_e32 v4, s4, v110
	v_ashrrev_i32_e32 v5, 31, v4
	v_lshlrev_b64 v[4:5], 12, v[4:5]
	v_lshl_add_u64 v[4:5], s[0:1], 0, v[4:5]
	v_ashrrev_i32_e32 v3, 31, v2
	v_lshl_add_u64 v[2:3], v[2:3], 2, v[4:5]
	s_movk_i32 s0, 0x2000
	v_add_co_u32_e32 v4, vcc, s0, v2
	s_movk_i32 s4, 0x4000
	s_nop 0
	v_addc_co_u32_e32 v5, vcc, 0, v3, vcc
	global_load_dwordx4 v[42:45], v[4:5], off offset:-4096 nt
	global_load_dwordx4 v[34:37], v[4:5], off nt
	v_add_co_u32_e32 v4, vcc, s4, v2
	s_movk_i32 s1, 0x5000
	s_nop 0
	v_addc_co_u32_e32 v5, vcc, 0, v3, vcc
	global_load_dwordx4 v[46:49], v[4:5], off offset:-4096 nt
	global_load_dwordx4 v[38:41], v[4:5], off nt
	v_add_co_u32_e32 v4, vcc, s1, v2
	s_add_i32 s5, s62, s2
	s_nop 0
	v_addc_co_u32_e32 v5, vcc, 0, v3, vcc
	global_load_dwordx4 v[62:65], v[2:3], off nt
	global_load_dwordx4 v[50:53], v[4:5], off nt
	v_add_co_u32_e32 v4, vcc, 0x6000, v2
	s_cmpk_gt_i32 s5, 0xaeb
	s_nop 0
	v_addc_co_u32_e32 v5, vcc, 0, v3, vcc
	v_add_co_u32_e32 v2, vcc, 0x7000, v2
	s_movk_i32 s1, 0x3000
	s_nop 0
	v_addc_co_u32_e32 v3, vcc, 0, v3, vcc
	global_load_dwordx4 v[58:61], v[4:5], off nt
	global_load_dwordx4 v[54:57], v[2:3], off nt
	s_cbranch_scc1 .LBB0_74
	s_ashr_i32 s6, s5, 31
	s_lshr_b32 s6, s6, 26
	s_add_i32 s7, s5, s6
	s_ashr_i32 s6, s7, 6
	s_and_b32 s7, s7, 0xffc0
	s_sub_i32 s5, s5, s7
	s_bfe_i32 s7, s5, 0x80000
	s_bfe_u32 s7, s7, 0x2000d
	s_add_i32 s7, s5, s7
	s_bfe_i32 s8, s7, 0x80000
	s_and_b32 s7, s7, 0xfc
	s_sub_i32 s5, s5, s7
	s_ashr_i32 s7, s6, 31
	s_lshl_b64 s[6:7], s[6:7], 22
	s_sext_i32_i16 s8, s8
	s_sext_i32_i8 s5, s5
	s_add_u32 s6, s72, s6
	v_lshl_or_b32 v2, s5, 8, v99
	s_addc_u32 s7, s73, s7
	s_lshl_b32 s5, s8, 4
	s_andn2_b32 s5, s5, 63
	v_or_b32_e32 v4, s5, v110
	v_ashrrev_i32_e32 v5, 31, v4
	v_lshlrev_b64 v[4:5], 12, v[4:5]
	v_lshl_add_u64 v[4:5], s[6:7], 0, v[4:5]
	v_ashrrev_i32_e32 v3, 31, v2
	v_lshl_add_u64 v[26:27], v[2:3], 2, v[4:5]
	v_add_co_u32_e32 v2, vcc, s0, v26
	s_nop 1
	v_addc_co_u32_e32 v3, vcc, 0, v27, vcc
	v_add_co_u32_e32 v10, vcc, s4, v26
	global_load_dwordx4 v[6:9], v[2:3], off offset:-4096 nt
	s_nop 0
	global_load_dwordx4 v[2:5], v[2:3], off nt
	v_addc_co_u32_e32 v11, vcc, 0, v27, vcc
	v_add_co_u32_e32 v18, vcc, 0x5000, v26
	global_load_dwordx4 v[14:17], v[10:11], off offset:-4096 nt
	s_nop 0
	global_load_dwordx4 v[10:13], v[10:11], off nt
	v_addc_co_u32_e32 v19, vcc, 0, v27, vcc
	v_add_co_u32_e32 v28, vcc, 0x6000, v26
	global_load_dwordx4 v[22:25], v[26:27], off nt
	s_nop 0
	global_load_dwordx4 v[18:21], v[18:19], off nt
	v_addc_co_u32_e32 v29, vcc, 0, v27, vcc
	v_add_co_u32_e32 v30, vcc, 0x7000, v26
	s_nop 1
	v_addc_co_u32_e32 v31, vcc, 0, v27, vcc
	global_load_dwordx4 v[26:29], v[28:29], off nt
	s_nop 0
	global_load_dwordx4 v[30:33], v[30:31], off nt

; __device__ __forceinline__ unsigned g8_cvt_pk(float lo, float hi) { unsigned r; asm volatile("v_cvt_pk_bf16_f32 %0, %1, %2" : "=v"(r) : "v"(lo), "v"(hi)); return r; }
; __device__ __forceinline__ void bt_load(const float* __restrict__ src, int N, int perm, int it, int ntn, f32x4 (&v)[8]) {
;     const int wid = threadIdx.x >> 6, lane = threadIdx.x & 63;
;     const int per = 16 * ntn, z = it / per, r = it % per, kt = r / ntn, nt = r % ntn;
;     const int np = nt * 256 + lane * 4;
;     const int sc = perm ? (nt * 128 + (lane & 31) * 4 + (lane >> 5) * 1024) : np;
;     const float* p = src + (size_t)z * 1024 * N + (size_t)(kt * 64 + wid * 8) * N + sc;
; #pragma unroll
;     for (int i = 0; i < 8; ++i) v[i] = __builtin_nontemporal_load((const f32x4*)(p + (size_t)i * N));
; __device__ __forceinline__ void ph_big_transpose(const float* __restrict__ src, int N, int perm, int batch, bf16* __restrict__ dst, float* tile  , int G, int ndefer) {
;     ...
;     for (; it < total; it += G) {
;         const bool more = it + G < total, more2 = it + 2 * G < total;
;         if (more2) bt_load(src, N, perm, it + 2 * G, ntn, nx2);
;         __syncthreads();
; #pragma unroll
;         for (int i = 0; i < 8; ++i) { float* t = tile + (wid * 8 + i) * 257 + lane * 4; t[0] = cur[i][0]; t[1] = cur[i][1]; t[2] = cur[i][2]; t[3] = cur[i][3]; }
;         __syncthreads();
;         const int per = 16 * ntn, z = it / per, r = it % per, kt = r / ntn, nt = r % ntn;
;         bf16* d = dst + (size_t)z * N * 1024 + (((size_t)nt * 16 + kt) << 14);
;         const int kc = lane & 7;
; #pragma unroll
;         for (int pss = 0; pss < 4; ++pss) {
;             const int n = wid * 32 + pss * 8 + (lane >> 3); float f[8];
; #pragma unroll
;             for (int j = 0; j < 8; ++j) f[j] = tile[(kc * 8 + j) * 257 + n];
;             u32x4 w; w.x = g8_cvt_pk(f[0], f[1]); w.y = g8_cvt_pk(f[2], f[3]); w.z = g8_cvt_pk(f[4], f[5]); w.w = g8_cvt_pk(f[6], f[7]);
;             __builtin_nontemporal_store(w, (u32x4*)(d + n * 64 + kc * 8));
;         }
;         if (more) {
; #pragma unroll
;             for (int i = 0; i < 8; ++i) { cur[i] = nxt[i]; nxt[i] = nx2[i]; } }
;     }
.LBB0_75:
	s_ashr_i32 s8, s3, 31
	s_barrier
	s_waitcnt vmcnt(3)
	ds_write_b128 v111, v[62:65]
	v_add_u32_e32 v62, 0x404, v111
	s_lshr_b32 s8, s8, 26
	ds_write2_b32 v62, v42, v43 offset1:1
	v_add_u32_e32 v42, 0x40c, v111
	s_add_i32 s9, s3, s8
	ds_write2_b32 v42, v44, v45 offset1:1
	v_add_u32_e32 v42, 0x808, v111
	s_ashr_i32 s8, s9, 6
	s_and_b32 s9, s9, 0xffc0
	s_add_i32 s7, s3, s62
	ds_write2_b64 v42, v[34:35], v[36:37] offset1:1
	v_add_u32_e32 v34, 0xc0c, v111
	s_sub_i32 s3, s3, s9
	ds_write2_b32 v34, v46, v47 offset1:1
	v_add_u32_e32 v34, 0xc14, v111
	s_bfe_i32 s9, s3, 0x80000
	ds_write2_b32 v34, v48, v49 offset1:1
	ds_write_b128 v111, v[38:41] offset:4112
	v_add_u32_e32 v34, 0x1414, v111
	s_bfe_u32 s9, s9, 0x2000d
	s_waitcnt vmcnt(2)
	ds_write2_b32 v34, v50, v51 offset1:1
	v_add_u32_e32 v34, 0x141c, v111
	s_add_i32 s9, s3, s9
	ds_write2_b32 v34, v52, v53 offset1:1
	v_add_u32_e32 v34, 0x1818, v111
	s_bfe_i32 s10, s9, 0x80000
	s_and_b32 s9, s9, 0xfc
	s_waitcnt vmcnt(1)
	ds_write2_b64 v34, v[58:59], v[60:61] offset1:1
	v_add_u32_e32 v34, 0x1c1c, v111
	s_sext_i32_i16 s10, s10
	s_sub_i32 s30, s3, s9
	s_ashr_i32 s9, s8, 31
	s_waitcnt vmcnt(0)
	ds_write2_b32 v34, v54, v55 offset1:1
	v_add_u32_e32 v34, 0x1c24, v111
	s_lshr_b32 s10, s10, 2
	s_lshl_b64 s[8:9], s[8:9], 21
	ds_write2_b32 v34, v56, v57 offset1:1
	s_waitcnt lgkmcnt(0)
	s_barrier
	s_add_u32 s3, s4, s8
	ds_read_b32 v34, v112 offset:1028
	ds_read_b32 v35, v112 offset:3084
	ds_read_b32 v36, v112 offset:5140
	ds_read_b32 v37, v112 offset:7196
	ds_read_b32 v38, v112 offset:6168
	ds_read_b32 v39, v112 offset:4112
	ds_read_b32 v40, v112 offset:2056
	ds_read_b32 v41, v112
	s_addc_u32 s31, s5, s9
	s_bfe_i64 s[8:9], s[30:31], 0x80000
	s_bfe_i64 s[10:11], s[10:11], 0x100000
	s_lshl_b64 s[8:9], s[8:9], 19
	s_add_u32 s3, s3, s8
	s_addc_u32 s30, s31, s9
	s_lshl_b64 s[8:9], s[10:11], 15
	s_waitcnt lgkmcnt(0)
	v_cvt_pk_bf16_f32 v34, v41, v34
	v_cvt_pk_bf16_f32 v35, v40, v35
	v_cvt_pk_bf16_f32 v36, v39, v36
	v_cvt_pk_bf16_f32 v37, v38, v37
	ds_read_b32 v42, v112 offset:1060
	ds_read_b32 v43, v112 offset:3116
	ds_read_b32 v44, v112 offset:5172
	ds_read_b32 v45, v112 offset:7228
	ds_read_b32 v46, v112 offset:6200
	ds_read_b32 v47, v112 offset:4144
	ds_read_b32 v48, v112 offset:2088
	ds_read_b32 v49, v112 offset:32
	s_add_u32 s8, s3, s8
	s_addc_u32 s9, s30, s9
	v_lshl_add_u64 v[38:39], s[8:9], 0, v[100:101]
	v_mov_b32_e32 v103, v101
	v_lshl_add_u64 v[40:41], v[38:39], 0, v[102:103]
	global_store_dwordx4 v[40:41], v[34:37], off nt
	v_mov_b32_e32 v105, v101
	v_lshl_add_u64 v[40:41], v[38:39], 0, v[104:105]
	s_waitcnt lgkmcnt(0)
	v_cvt_pk_bf16_f32 v34, v49, v42
	v_cvt_pk_bf16_f32 v35, v48, v43
	v_cvt_pk_bf16_f32 v36, v47, v44
	v_cvt_pk_bf16_f32 v37, v46, v45
	ds_read_b32 v42, v112 offset:1092
	ds_read_b32 v43, v112 offset:3148
	ds_read_b32 v44, v112 offset:5204
	ds_read_b32 v45, v112 offset:6232
	ds_read_b32 v46, v112 offset:4176
	ds_read_b32 v47, v112 offset:2120
	ds_read_b32 v48, v112 offset:64
	ds_read_b32 v49, v112 offset:7260
	global_store_dwordx4 v[40:41], v[34:37], off nt
	v_mov_b32_e32 v107, v101
	v_lshl_add_u64 v[40:41], v[38:39], 0, v[106:107]
	s_waitcnt lgkmcnt(1)
	v_cvt_pk_bf16_f32 v34, v48, v42
	v_cvt_pk_bf16_f32 v35, v47, v43
	v_cvt_pk_bf16_f32 v36, v46, v44
	s_waitcnt lgkmcnt(0)
	v_cvt_pk_bf16_f32 v37, v45, v49
	ds_read_b32 v42, v112 offset:1124
	ds_read_b32 v43, v112 offset:3180
	ds_read_b32 v44, v112 offset:5236
	ds_read_b32 v45, v112 offset:6264
	ds_read_b32 v46, v112 offset:4208
	ds_read_b32 v47, v112 offset:2152
	ds_read_b32 v48, v112 offset:96
	ds_read_b32 v49, v112 offset:7292
	v_mov_b32_e32 v109, v101
	global_store_dwordx4 v[40:41], v[34:37], off nt
	v_lshl_add_u64 v[38:39], v[38:39], 0, v[108:109]
	v_mov_b64_e32 v[56:57], v[32:33]
	s_waitcnt lgkmcnt(1)
	v_cvt_pk_bf16_f32 v34, v48, v42
	v_cvt_pk_bf16_f32 v35, v47, v43
	v_cvt_pk_bf16_f32 v36, v46, v44
	s_waitcnt lgkmcnt(0)
	v_cvt_pk_bf16_f32 v37, v45, v49
	global_store_dwordx4 v[38:39], v[34:37], off nt
	v_mov_b64_e32 v[60:61], v[28:29]
	v_mov_b64_e32 v[52:53], v[20:21]
	v_mov_b64_e32 v[40:41], v[12:13]
	v_mov_b64_e32 v[48:49], v[16:17]
	v_mov_b64_e32 v[36:37], v[4:5]
	v_mov_b64_e32 v[44:45], v[8:9]
	v_mov_b64_e32 v[64:65], v[24:25]
	v_mov_b64_e32 v[54:55], v[30:31]
	v_mov_b64_e32 v[58:59], v[26:27]
	v_mov_b64_e32 v[50:51], v[18:19]
	v_mov_b64_e32 v[38:39], v[10:11]
	v_mov_b64_e32 v[46:47], v[14:15]
	v_mov_b64_e32 v[34:35], v[2:3]
	v_mov_b64_e32 v[42:43], v[6:7]
	v_mov_b64_e32 v[62:63], v[22:23]
	v_mov_b64_e32 v[30:31], v[94:95]
	v_mov_b64_e32 v[26:27], v[90:91]
	v_mov_b64_e32 v[18:19], v[86:87]
	v_mov_b64_e32 v[10:11], v[82:83]
	v_mov_b64_e32 v[14:15], v[74:75]
	v_mov_b64_e32 v[2:3], v[66:67]
	v_mov_b64_e32 v[6:7], v[70:71]
	v_mov_b64_e32 v[22:23], v[78:79]
	s_cmpk_lt_i32 s7, 0xaec
	v_mov_b64_e32 v[32:33], v[96:97]
	v_mov_b64_e32 v[28:29], v[92:93]
	v_mov_b64_e32 v[20:21], v[88:89]
	v_mov_b64_e32 v[12:13], v[84:85]
	v_mov_b64_e32 v[16:17], v[76:77]
	v_mov_b64_e32 v[4:5], v[68:69]
	v_mov_b64_e32 v[8:9], v[72:73]
	v_mov_b64_e32 v[24:25], v[80:81]
	s_mov_b32 s3, s7
	s_cbranch_scc0 .LBB0_78
.LBB0_76:
	s_add_i32 s7, s6, s3
	s_cmpk_gt_i32 s7, 0xaeb
	s_cbranch_scc1 .LBB0_75
	s_ashr_i32 s8, s7, 31
	s_lshr_b32 s8, s8, 26
	s_add_i32 s9, s7, s8
	s_ashr_i32 s8, s9, 6
	s_and_b32 s9, s9, 0xffc0
	s_sub_i32 s7, s7, s9
	s_bfe_i32 s9, s7, 0x80000
	s_bfe_u32 s9, s9, 0x2000d
	s_add_i32 s9, s7, s9
	s_bfe_i32 s10, s9, 0x80000
	s_and_b32 s9, s9, 0xfc
	s_sub_i32 s7, s7, s9
	s_ashr_i32 s9, s8, 31
	s_lshl_b64 s[8:9], s[8:9], 22
	s_sext_i32_i16 s10, s10
	s_sext_i32_i8 s7, s7
	s_add_u32 s8, s72, s8
	v_lshl_or_b32 v66, s7, 8, v99
	s_addc_u32 s9, s73, s9
	s_lshl_b32 s7, s10, 4
	s_andn2_b32 s7, s7, 63
	v_or_b32_e32 v68, s7, v110
	v_ashrrev_i32_e32 v69, 31, v68
	v_lshlrev_b64 v[68:69], 12, v[68:69]
	v_lshl_add_u64 v[68:69], s[8:9], 0, v[68:69]
	v_ashrrev_i32_e32 v67, 31, v66
	v_lshl_add_u64 v[90:91], v[66:67], 2, v[68:69]
	v_add_co_u32_e32 v66, vcc, s0, v90
	s_nop 1
	v_addc_co_u32_e32 v67, vcc, 0, v91, vcc
	v_add_co_u32_e32 v74, vcc, s1, v90
	global_load_dwordx4 v[70:73], v[66:67], off offset:-4096 nt
	s_nop 0
	global_load_dwordx4 v[66:69], v[66:67], off nt
	v_addc_co_u32_e32 v75, vcc, 0, v91, vcc
	v_add_co_u32_e32 v82, vcc, 0x4000, v90
	global_load_dwordx4 v[78:81], v[90:91], off nt
	s_nop 0
	global_load_dwordx4 v[74:77], v[74:75], off nt
	v_addc_co_u32_e32 v83, vcc, 0, v91, vcc
	v_add_co_u32_e32 v86, vcc, 0x5000, v90
	s_nop 1
	v_addc_co_u32_e32 v87, vcc, 0, v91, vcc
	v_add_co_u32_e32 v92, vcc, 0x6000, v90
	global_load_dwordx4 v[82:85], v[82:83], off nt
	s_nop 0
	global_load_dwordx4 v[86:89], v[86:87], off nt
	v_addc_co_u32_e32 v93, vcc, 0, v91, vcc
	v_add_co_u32_e32 v94, vcc, 0x7000, v90
	s_nop 1
	v_addc_co_u32_e32 v95, vcc, 0, v91, vcc
	global_load_dwordx4 v[90:93], v[92:93], off nt
	s_nop 0
	global_load_dwordx4 v[94:97], v[94:95], off nt
	s_branch .LBB0_75

; #define SEAM(k) do { if (IN(k) && IN((k) + 1)) xcd_barrier(bar); \
;         if (PROBE_MASK) { const unsigned long long t_ = __builtin_amdgcn_s_memrealtime(); if ((PROBE_MASK >> (k)) & 1u) pr_acc += t_ - pr_t0; pr_t0 = t_; } } while (0)
; __device__ __forceinline__ void convert_deferred(const Ptrs& P, unsigned char* lds, int quota) {
;     const int tid = threadIdx.x, wid = tid >> 6, lane = tid & 63;
;     float* tile = (float*)lds;
;     volatile __attribute__((address_space(3))) int* slot = (volatile __attribute__((address_space(3))) int*)((__attribute__((address_space(3))) unsigned char*)lds + 131072 + 320 + 11000);
;     unsigned* q = (unsigned*)(P.ws + WS_CTL) + CW_DEFQ;
;     for (int n = 0; n < quota; ++n) {
;         __syncthreads();
;         if (tid == 0) *slot = (int)atomicAdd(q, 1u);
;         __syncthreads();
;         const int t = *slot;
;         if (t >= DEF_GU + DEF_DN) break;
;         const bool gu = t < DEF_GU;
;         const float* src = gu ? P.in[34] : P.in[36]; bf16* dst = (bf16*)(P.ws + (gu ? WS_WGU : WS_WDN));
;         const int N = gu ? 2048 : 1024, ntn = N / 256, it = gu ? 2 * NE * 16 * 8 - DEF_GU + t : 2 * NE * 16 * 4 - DEF_DN + (t - DEF_GU);
; __global__ void __launch_bounds__(NT, 2) mega(Args args) {
;     ...
;     if (IN(2)) { g8::DenseOrder S; S.init(H, D, (const bf16*)(ws + WS_WEVIN), D, R, EVEN_IN_P, G, (int)blockIdx.x, 0); g8::EpiStoreBf16 E{Z, EVEN_IN_P};
;         g8::gemm_phase<g8::EpiStoreBf16, g8::DenseOrder, false, true>(LDSP, D, D, S, E);
;         if (IDLE_LAST(68 * 7)) convert_deferred(P, lds, 4); } SEAM(2);
.LBB0_779:
	s_abs_i32 s3, s62
	v_cvt_f32_u32_e32 v2, s3
	s_sub_i32 s4, 0, s3
	s_mov_b32 s5, 0
	v_rcp_iflag_f32_e32 v2, v2
	s_nop 0
	v_mul_f32_e32 v2, 0x4f7ffffe, v2
	v_cvt_u32_f32_e32 v2, v2
	s_nop 0
	v_readfirstlane_b32 s6, v2
	s_mul_i32 s4, s4, s6
	s_mul_hi_u32 s4, s6, s4
	s_add_i32 s6, s6, s4
	s_mul_hi_u32 s4, s6, 0x1dc
	s_mul_i32 s4, s4, s3
	s_sub_i32 s4, 0x1dc, s4
	s_sub_i32 s6, s4, s3
	s_cmp_ge_u32 s4, s3
	s_cselect_b32 s4, s6, s4
	s_sub_i32 s6, s4, s3
	s_cmp_ge_u32 s4, s3
	s_cselect_b32 s3, s6, s4
	s_cmp_eq_u32 s3, 0
	s_cselect_b64 s[6:7], -1, 0
	s_cmp_lt_i32 s2, s3
	s_cselect_b64 s[8:9], -1, 0
	s_or_b64 s[6:7], s[6:7], s[8:9]
	s_and_b64 vcc, exec, s[6:7]
	s_cbranch_vccnz .LBB0_789
	v_and_b32_e32 v2, 0x7c, v155
	v_lshlrev_b32_e32 v3, 5, v0
	s_movk_i32 s3, 0x400
	v_lshrrev_b32_e32 v4, 6, v0
	v_and_or_b32 v12, v3, s3, v2
	v_bfe_u32 v2, v0, 3, 3
	v_lshl_or_b32 v5, v4, 5, v2
	v_lshlrev_b32_e32 v2, 3, v0
	v_lshl_add_u32 v11, v182, 4, 0
	v_and_b32_e32 v2, 56, v2
	v_mul_u32_u24_e32 v16, 0x2020, v4
	v_mov_b32_e32 v3, 0
	v_lshl_add_u32 v27, v5, 2, 0
	v_mul_u32_u24_e32 v28, 0x404, v2
	v_lshlrev_b32_e32 v10, 6, v5
	s_add_i32 s12, 0, 0x22c38
	v_add_u32_e32 v16, v11, v16
	v_and_b32_e32 v13, 0xfc, v155
	v_and_b32_e32 v14, 56, v154
	s_mov_b32 s3, 6
	v_or_b32_e32 v4, 0x200, v10
	v_mov_b32_e32 v5, v3
	v_or_b32_e32 v6, 0x400, v10
	v_mov_b32_e32 v7, v3
	v_or_b32_e32 v8, 0x600, v10
	v_mov_b32_e32 v9, v3
	v_mov_b32_e32 v15, s12
	s_movk_i32 s13, 0xf3b
	s_movk_i32 s14, 0x800
	s_mov_b32 s15, 0x1104e000
	s_movk_i32 s16, 0xc4
	v_add_u32_e32 v17, 0x404, v16
	v_add_u32_e32 v18, 0x40c, v16
	v_add_u32_e32 v19, 0x808, v16
	v_add_u32_e32 v20, 0xc0c, v16
	v_add_u32_e32 v21, 0xc14, v16
	v_add_u32_e32 v22, 0x1414, v16
	v_add_u32_e32 v23, 0x141c, v16
	v_add_u32_e32 v24, 0x1818, v16
	v_add_u32_e32 v25, 0x1c1c, v16
	v_add_u32_e32 v26, 0x1c24, v16
	v_lshlrev_b32_e32 v2, 1, v2
	v_add_u32_e32 v27, v27, v28
	v_lshlrev_b32_e32 v10, 1, v10
	s_branch .LBB0_782

; __device__ __forceinline__ unsigned g8_cvt_pk(float lo, float hi) { unsigned r; asm volatile("v_cvt_pk_bf16_f32 %0, %1, %2" : "=v"(r) : "v"(lo), "v"(hi)); return r; }
; __device__ __forceinline__ void convert_deferred(const Ptrs& P, unsigned char* lds, int quota) {
;     ...
;         __syncthreads();
;         if (tid == 0) *slot = (int)atomicAdd(q, 1u);
;         __syncthreads();
;         const int t = *slot;
;         if (t >= DEF_GU + DEF_DN) break;
;         const bool gu = t < DEF_GU;
;         const float* src = gu ? P.in[34] : P.in[36]; bf16* dst = (bf16*)(P.ws + (gu ? WS_WGU : WS_WDN));
;         const int N = gu ? 2048 : 1024, ntn = N / 256, it = gu ? 2 * NE * 16 * 8 - DEF_GU + t : 2 * NE * 16 * 4 - DEF_DN + (t - DEF_GU);
;         f32x4 cur[8];
;         bt_load(src, N, gu ? 1 : 0, it, ntn, cur);
; #pragma unroll
;         for (int i = 0; i < 8; ++i) { float* tp = tile + (wid * 8 + i) * 257 + lane * 4; tp[0] = cur[i][0]; tp[1] = cur[i][1]; tp[2] = cur[i][2]; tp[3] = cur[i][3]; }
;         __syncthreads();
;         const int per = 16 * ntn, z = it / per, r = it % per, kt = r / ntn, nt = r % ntn;
;         bf16* d = dst + (size_t)z * N * 1024 + (((size_t)nt * 16 + kt) << 14);
;         const int kc = lane & 7;
; #pragma unroll
;         for (int pss = 0; pss < 4; ++pss) {
;             const int nn = wid * 32 + pss * 8 + (lane >> 3); float f[8];
; #pragma unroll
;             for (int j = 0; j < 8; ++j) f[j] = tile[(kc * 8 + j) * 257 + nn];
;             u32x4 w; w.x = g8_cvt_pk(f[0], f[1]); w.y = g8_cvt_pk(f[2], f[3]); w.z = g8_cvt_pk(f[4], f[5]); w.w = g8_cvt_pk(f[6], f[7]);
;             *(u32x4*)(d + nn * 64 + kc * 8) = w;
;         }
.LBB0_786:
	s_or_b64 exec, exec, s[6:7]
	s_waitcnt lgkmcnt(0)
	s_barrier
	ds_read_b32 v11, v15
	s_mov_b64 s[6:7], -1
	s_waitcnt lgkmcnt(0)
	v_cmp_lt_i32_e32 vcc, s13, v11
	v_readfirstlane_b32 s4, v11
	s_cbranch_vccnz .LBB0_781
	s_cmpk_gt_i32 s4, 0xa27
	s_cselect_b64 vcc, -1, 0
	s_and_b64 s[6:7], vcc, exec
	s_cselect_b32 s6, s15, 0x104e000
	s_cselect_b32 s11, 0x400, s14
	s_cselect_b32 s17, s73, s69
	s_cselect_b32 s20, s72, s68
	s_cselect_b32 s7, s16, 0x15d8
	s_cselect_b32 s18, 20, 21
	s_cselect_b32 s21, 10, 11
	s_add_u32 s26, s78, s6
	s_addc_u32 s27, s79, 0
	s_lshr_b32 s8, s11, 4
	s_abs_i32 s6, s8
	v_cvt_f32_u32_e32 v11, s6
	s_sub_i32 s19, 0, s6
	s_add_i32 s7, s7, s4
	s_abs_i32 s9, s7
	v_rcp_iflag_f32_e32 v11, v11
	s_xor_b32 s4, s7, s8
	s_lshr_b32 s10, s11, 8
	s_ashr_i32 s4, s4, 31
	v_mul_f32_e32 v11, 0x4f7ffffe, v11
	v_cvt_u32_f32_e32 v11, v11
	s_nop 0
	v_readfirstlane_b32 s28, v11
	s_mul_i32 s19, s19, s28
	s_mul_hi_u32 s19, s28, s19
	s_add_i32 s28, s28, s19
	s_mul_hi_u32 s19, s9, s28
	s_mul_i32 s28, s19, s6
	s_sub_i32 s9, s9, s28
	s_add_i32 s28, s19, 1
	s_sub_i32 s29, s9, s6
	s_cmp_ge_u32 s9, s6
	s_cselect_b32 s19, s28, s19
	s_cselect_b32 s9, s29, s9
	s_add_i32 s28, s19, 1
	s_cmp_ge_u32 s9, s6
	s_cselect_b32 s6, s28, s19
	s_xor_b32 s6, s6, s4
	s_sub_i32 s6, s6, s4
	s_sext_i32_i8 s4, s10
	v_cvt_f32_i32_e32 v11, s4
	s_mul_i32 s8, s6, s8
	s_sub_i32 s7, s7, s8
	v_cvt_f32_i32_e32 v28, s7
	v_rcp_iflag_f32_e32 v29, v11
	s_xor_b32 s4, s7, s4
	s_ashr_i32 s4, s4, 30
	s_or_b32 s4, s4, 1
	v_mul_f32_e32 v29, v28, v29
	v_trunc_f32_e32 v29, v29
	v_fma_f32 v28, -v29, v11, v28
	v_cvt_i32_f32_e32 v29, v29
	v_cmp_ge_f32_e64 s[8:9], |v28|, |v11|
	s_and_b64 s[8:9], s[8:9], exec
	s_cselect_b32 s4, s4, 0
	v_readfirstlane_b32 s8, v29
	s_add_i32 s8, s8, s4
	s_mul_i32 s9, s8, s10
	s_sub_i32 s10, s7, s9
	s_sext_i32_i8 s7, s10
	v_lshl_add_u32 v11, s7, 7, v12
	v_lshl_or_b32 v28, s7, 8, v13
	s_ashr_i32 s7, s6, 31
	s_sext_i32_i8 s4, s8
	s_lshl_b64 s[18:19], s[6:7], s18
	v_lshl_or_b32 v30, s4, 6, v14
	s_lshl_b64 s[18:19], s[18:19], 2
	v_ashrrev_i32_e32 v31, 31, v30
	s_add_u32 s18, s20, s18
	v_cndmask_b32_e32 v28, v11, v28, vcc
	s_addc_u32 s19, s17, s19
	v_lshlrev_b64 v[30:31], s21, v[30:31]
	v_lshl_add_u64 v[30:31], v[30:31], 2, s[18:19]
	v_ashrrev_i32_e32 v29, 31, v28
	v_lshl_add_u64 v[52:53], v[28:29], 2, v[30:31]
	s_lshl_b64 s[18:19], 12, s21
	s_lshl_b32 s4, s11, 2
	v_lshl_add_u64 v[40:41], v[52:53], 0, s[18:19]
	s_lshl_b64 s[18:19], 24, s21
	v_lshl_add_u64 v[36:37], v[52:53], 0, s[4:5]
	v_lshl_add_u64 v[44:45], v[52:53], 0, s[18:19]
	s_lshl_b64 s[18:19], 28, s21
	v_lshl_add_u64 v[54:55], v[36:37], 0, s[4:5]
	v_lshl_add_u64 v[48:49], v[52:53], 0, s[18:19]
	s_lshl_b32 s4, s11, 3
	s_lshl_b64 s[18:19], 20, s21
	global_load_dwordx4 v[28:31], v[52:53], off nt
	global_load_dwordx4 v[32:35], v[36:37], off nt
	s_nop 0
	global_load_dwordx4 v[36:39], v[54:55], off nt
	s_nop 0
	global_load_dwordx4 v[40:43], v[40:41], off nt
	v_lshl_add_u64 v[54:55], v[54:55], 0, s[4:5]
	v_lshl_add_u64 v[56:57], v[52:53], 0, s[18:19]
	global_load_dwordx4 v[44:47], v[44:45], off nt
	s_nop 0
	global_load_dwordx4 v[48:51], v[48:49], off nt
	s_nop 0
	global_load_dwordx4 v[52:55], v[54:55], off nt
	s_nop 0
	global_load_dwordx4 v[56:59], v[56:57], off nt
	s_lshl_b64 s[6:7], s[6:7], s21
	s_lshl_b64 s[6:7], s[6:7], 11
	s_add_u32 s4, s26, s6
	s_addc_u32 s11, s27, s7
	s_bfe_i64 s[6:7], s[10:11], 0x80000
	s_bfe_i64 s[8:9], s[8:9], 0x80000
	s_lshl_b64 s[6:7], s[6:7], 19
	s_add_u32 s4, s4, s6
	s_addc_u32 s10, s11, s7
	s_lshl_b64 s[6:7], s[8:9], 15
	s_add_u32 s6, s4, s6
	s_addc_u32 s7, s10, s7
	v_mov_b32_e32 v11, v3
	s_add_i32 s3, s3, -1
	s_cmp_eq_u32 s3, 0
	s_waitcnt vmcnt(7)
	ds_write_b128 v16, v[28:31]
	s_waitcnt vmcnt(6)
	ds_write2_b32 v17, v32, v33 offset1:1
	ds_write2_b32 v18, v34, v35 offset1:1
	s_waitcnt vmcnt(3)
	ds_write2_b64 v24, v[44:45], v[46:47] offset1:1
	s_waitcnt vmcnt(2)
	ds_write2_b32 v25, v48, v49 offset1:1
	ds_write2_b32 v26, v50, v51 offset1:1
	ds_write2_b64 v19, v[36:37], v[38:39] offset1:1
	ds_write2_b32 v20, v40, v41 offset1:1
	ds_write2_b32 v21, v42, v43 offset1:1
	s_waitcnt vmcnt(1)
	ds_write_b128 v16, v[52:55] offset:4112
	s_waitcnt vmcnt(0)
	ds_write2_b32 v22, v56, v57 offset1:1
	ds_write2_b32 v23, v58, v59 offset1:1
	s_waitcnt lgkmcnt(0)
	s_barrier
	ds_read_b32 v28, v27 offset:1028
	ds_read_b32 v29, v27 offset:3084
	ds_read_b32 v30, v27 offset:5140
	ds_read_b32 v31, v27 offset:7196
	ds_read_b32 v32, v27 offset:6168
	ds_read_b32 v33, v27 offset:4112
	ds_read_b32 v34, v27 offset:2056
	ds_read_b32 v35, v27
	s_waitcnt lgkmcnt(0)
	v_cvt_pk_bf16_f32 v28, v35, v28
	v_cvt_pk_bf16_f32 v29, v34, v29
	v_cvt_pk_bf16_f32 v30, v33, v30
	v_cvt_pk_bf16_f32 v31, v32, v31
	ds_read_b32 v36, v27 offset:1060
	ds_read_b32 v37, v27 offset:3116
	ds_read_b32 v38, v27 offset:5172
	ds_read_b32 v39, v27 offset:7228
	ds_read_b32 v40, v27 offset:6200
	ds_read_b32 v41, v27 offset:4144
	ds_read_b32 v42, v27 offset:2088
	ds_read_b32 v43, v27 offset:32
	v_lshl_add_u64 v[32:33], s[6:7], 0, v[2:3]
	v_lshl_add_u64 v[34:35], v[32:33], 0, v[10:11]
	global_store_dwordx4 v[34:35], v[28:31], off
	v_lshl_add_u64 v[34:35], v[4:5], 1, v[32:33]
	s_cselect_b64 s[6:7], -1, 0
	s_waitcnt lgkmcnt(0)
	v_cvt_pk_bf16_f32 v28, v43, v36
	v_cvt_pk_bf16_f32 v29, v42, v37
	v_cvt_pk_bf16_f32 v30, v41, v38
	v_cvt_pk_bf16_f32 v31, v40, v39
	ds_read_b32 v11, v27 offset:1092
	ds_read_b32 v36, v27 offset:3148
	ds_read_b32 v37, v27 offset:6232
	ds_read_b32 v38, v27 offset:4176
	ds_read_b32 v39, v27 offset:2120
	ds_read_b32 v40, v27 offset:64
	ds_read_b32 v41, v27 offset:5204
	ds_read_b32 v42, v27 offset:7260
	global_store_dwordx4 v[34:35], v[28:31], off
	v_lshl_add_u64 v[34:35], v[6:7], 1, v[32:33]
	v_lshl_add_u64 v[32:33], v[8:9], 1, v[32:33]
	s_waitcnt lgkmcnt(2)
	v_cvt_pk_bf16_f32 v28, v40, v11
	v_cvt_pk_bf16_f32 v29, v39, v36
	s_waitcnt lgkmcnt(1)
	v_cvt_pk_bf16_f32 v30, v38, v41
	s_waitcnt lgkmcnt(0)
	v_cvt_pk_bf16_f32 v31, v37, v42
	ds_read_b32 v11, v27 offset:1124
	ds_read_b32 v36, v27 offset:3180
	ds_read_b32 v37, v27 offset:6264
	ds_read_b32 v38, v27 offset:4208
	ds_read_b32 v39, v27 offset:2152
	ds_read_b32 v40, v27 offset:96
	ds_read_b32 v41, v27 offset:5236
	ds_read_b32 v42, v27 offset:7292
	global_store_dwordx4 v[34:35], v[28:31], off
	s_waitcnt lgkmcnt(2)
	s_nop 0
	v_cvt_pk_bf16_f32 v28, v40, v11
	v_cvt_pk_bf16_f32 v29, v39, v36
	s_waitcnt lgkmcnt(1)
	v_cvt_pk_bf16_f32 v30, v38, v41
	s_waitcnt lgkmcnt(0)
	v_cvt_pk_bf16_f32 v31, v37, v42
	global_store_dwordx4 v[32:33], v[28:31], off
	s_branch .LBB0_781

; #define SEAM(k) do { if (IN(k) && IN((k) + 1)) xcd_barrier(bar); \
;         if (PROBE_MASK) { const unsigned long long t_ = __builtin_amdgcn_s_memrealtime(); if ((PROBE_MASK >> (k)) & 1u) pr_acc += t_ - pr_t0; pr_t0 = t_; } } while (0)
; __device__ __forceinline__ void convert_deferred(const Ptrs& P, unsigned char* lds, int quota) {
;     const int tid = threadIdx.x, wid = tid >> 6, lane = tid & 63;
;     float* tile = (float*)lds;
;     volatile __attribute__((address_space(3))) int* slot = (volatile __attribute__((address_space(3))) int*)((__attribute__((address_space(3))) unsigned char*)lds + 131072 + 320 + 11000);
;     unsigned* q = (unsigned*)(P.ws + WS_CTL) + CW_DEFQ;
;     for (int n = 0; n < quota; ++n) {
;         __syncthreads();
;         if (tid == 0) *slot = (int)atomicAdd(q, 1u);
;         __syncthreads();
;         const int t = *slot;
;         if (t >= DEF_GU + DEF_DN) break;
;         const bool gu = t < DEF_GU;
;         const float* src = gu ? P.in[34] : P.in[36]; bf16* dst = (bf16*)(P.ws + (gu ? WS_WGU : WS_WDN));
;         const int N = gu ? 2048 : 1024, ntn = N / 256, it = gu ? 2 * NE * 16 * 8 - DEF_GU + t : 2 * NE * 16 * 4 - DEF_DN + (t - DEF_GU);
; __global__ void __launch_bounds__(NT, 2) mega(Args args) {
;     ...
;     if (IN(6)) { g8::DenseOrder S; S.init(MIX, D, (const bf16*)(ws + WS_WEVOUT), D, R, D, G, (int)blockIdx.x, 0); g8::EpiOut E{P, 0};
;         g8::gemm_phase<g8::EpiOut, g8::DenseOrder, false, true>(LDSP, D, D, S, E);
;         if (IDLE_LAST(68 * 4)) convert_deferred(P, lds, 4); } SEAM(6);
.LBB0_1286:
	s_abs_i32 s3, s62
	v_cvt_f32_u32_e32 v2, s3
	s_sub_i32 s4, 0, s3
	s_mov_b32 s5, 0
	v_rcp_iflag_f32_e32 v2, v2
	s_nop 0
	v_mul_f32_e32 v2, 0x4f7ffffe, v2
	v_cvt_u32_f32_e32 v2, v2
	s_nop 0
	v_readfirstlane_b32 s6, v2
	s_mul_i32 s4, s4, s6
	s_mul_hi_u32 s4, s6, s4
	s_add_i32 s6, s6, s4
	s_mul_hi_u32 s4, s6, 0x110
	s_mul_i32 s4, s4, s3
	s_sub_i32 s4, 0x110, s4
	s_sub_i32 s6, s4, s3
	s_cmp_ge_u32 s4, s3
	s_cselect_b32 s4, s6, s4
	s_sub_i32 s6, s4, s3
	s_cmp_ge_u32 s4, s3
	s_cselect_b32 s3, s6, s4
	s_cmp_eq_u32 s3, 0
	s_cselect_b64 s[6:7], -1, 0
	s_cmp_lt_i32 s2, s3
	s_cselect_b64 s[8:9], -1, 0
	s_or_b64 s[6:7], s[6:7], s[8:9]
	s_and_b64 vcc, exec, s[6:7]
	s_cbranch_vccnz .LBB0_1296
	v_and_b32_e32 v2, 0x7c, v188
	v_lshlrev_b32_e32 v3, 5, v0
	s_movk_i32 s3, 0x400
	v_and_or_b32 v12, v3, s3, v2
	v_bfe_u32 v2, v0, 3, 3
	v_lshl_or_b32 v4, v1, 5, v2
	v_lshlrev_b32_e32 v2, 3, v0
	v_lshl_add_u32 v11, v182, 4, 0
	v_and_b32_e32 v2, 56, v2
	v_mul_u32_u24_e32 v16, 0x2020, v1
	v_mov_b32_e32 v3, 0
	v_lshl_add_u32 v27, v4, 2, 0
	v_mul_u32_u24_e32 v28, 0x404, v2
	v_lshlrev_b32_e32 v10, 6, v4
	s_add_i32 s12, 0, 0x22c38
	v_add_u32_e32 v16, v11, v16
	v_and_b32_e32 v13, 0xfc, v188
	v_and_b32_e32 v14, 56, v185
	s_mov_b32 s3, 8
	v_or_b32_e32 v4, 0x200, v10
	v_mov_b32_e32 v5, v3
	v_or_b32_e32 v6, 0x400, v10
	v_mov_b32_e32 v7, v3
	v_or_b32_e32 v8, 0x600, v10
	v_mov_b32_e32 v9, v3
	v_mov_b32_e32 v15, s12
	s_movk_i32 s13, 0xf3b
	s_movk_i32 s14, 0x800
	s_mov_b32 s15, 0x1104e000
	s_movk_i32 s16, 0xc4
	v_add_u32_e32 v17, 0x404, v16
	v_add_u32_e32 v18, 0x40c, v16
	v_add_u32_e32 v19, 0x808, v16
	v_add_u32_e32 v20, 0xc0c, v16
	v_add_u32_e32 v21, 0xc14, v16
	v_add_u32_e32 v22, 0x1414, v16
	v_add_u32_e32 v23, 0x141c, v16
	v_add_u32_e32 v24, 0x1818, v16
	v_add_u32_e32 v25, 0x1c1c, v16
	v_add_u32_e32 v26, 0x1c24, v16
	v_lshlrev_b32_e32 v2, 1, v2
	v_add_u32_e32 v27, v27, v28
	v_lshlrev_b32_e32 v10, 1, v10
	s_branch .LBB0_1289

; __device__ __forceinline__ unsigned g8_cvt_pk(float lo, float hi) { unsigned r; asm volatile("v_cvt_pk_bf16_f32 %0, %1, %2" : "=v"(r) : "v"(lo), "v"(hi)); return r; }
; __device__ __forceinline__ void convert_deferred(const Ptrs& P, unsigned char* lds, int quota) {
;     ...
;         __syncthreads();
;         if (tid == 0) *slot = (int)atomicAdd(q, 1u);
;         __syncthreads();
;         const int t = *slot;
;         if (t >= DEF_GU + DEF_DN) break;
;         const bool gu = t < DEF_GU;
;         const float* src = gu ? P.in[34] : P.in[36]; bf16* dst = (bf16*)(P.ws + (gu ? WS_WGU : WS_WDN));
;         const int N = gu ? 2048 : 1024, ntn = N / 256, it = gu ? 2 * NE * 16 * 8 - DEF_GU + t : 2 * NE * 16 * 4 - DEF_DN + (t - DEF_GU);
;         f32x4 cur[8];
;         bt_load(src, N, gu ? 1 : 0, it, ntn, cur);
; #pragma unroll
;         for (int i = 0; i < 8; ++i) { float* tp = tile + (wid * 8 + i) * 257 + lane * 4; tp[0] = cur[i][0]; tp[1] = cur[i][1]; tp[2] = cur[i][2]; tp[3] = cur[i][3]; }
;         __syncthreads();
;         const int per = 16 * ntn, z = it / per, r = it % per, kt = r / ntn, nt = r % ntn;
;         bf16* d = dst + (size_t)z * N * 1024 + (((size_t)nt * 16 + kt) << 14);
;         const int kc = lane & 7;
; #pragma unroll
;         for (int pss = 0; pss < 4; ++pss) {
;             const int nn = wid * 32 + pss * 8 + (lane >> 3); float f[8];
; #pragma unroll
;             for (int j = 0; j < 8; ++j) f[j] = tile[(kc * 8 + j) * 257 + nn];
;             u32x4 w; w.x = g8_cvt_pk(f[0], f[1]); w.y = g8_cvt_pk(f[2], f[3]); w.z = g8_cvt_pk(f[4], f[5]); w.w = g8_cvt_pk(f[6], f[7]);
;             *(u32x4*)(d + nn * 64 + kc * 8) = w;
;         }
.LBB0_1293:
	s_or_b64 exec, exec, s[6:7]
	s_waitcnt lgkmcnt(0)
	s_barrier
	ds_read_b32 v11, v15
	s_mov_b64 s[6:7], -1
	s_waitcnt lgkmcnt(0)
	v_cmp_lt_i32_e32 vcc, s13, v11
	v_readfirstlane_b32 s4, v11
	s_cbranch_vccnz .LBB0_1288
	s_cmpk_gt_i32 s4, 0xa27
	s_cselect_b64 vcc, -1, 0
	s_and_b64 s[6:7], vcc, exec
	s_cselect_b32 s6, s15, 0x104e000
	s_cselect_b32 s11, 0x400, s14
	s_cselect_b32 s17, s73, s69
	s_cselect_b32 s20, s72, s68
	s_cselect_b32 s7, s16, 0x15d8
	s_cselect_b32 s18, 20, 21
	s_cselect_b32 s21, 10, 11
	s_add_u32 s22, s78, s6
	s_addc_u32 s23, s79, 0
	s_lshr_b32 s8, s11, 4
	s_abs_i32 s6, s8
	v_cvt_f32_u32_e32 v11, s6
	s_sub_i32 s19, 0, s6
	s_add_i32 s7, s7, s4
	s_abs_i32 s9, s7
	v_rcp_iflag_f32_e32 v11, v11
	s_xor_b32 s4, s7, s8
	s_lshr_b32 s10, s11, 8
	s_ashr_i32 s4, s4, 31
	v_mul_f32_e32 v11, 0x4f7ffffe, v11
	v_cvt_u32_f32_e32 v11, v11
	s_nop 0
	v_readfirstlane_b32 s24, v11
	s_mul_i32 s19, s19, s24
	s_mul_hi_u32 s19, s24, s19
	s_add_i32 s24, s24, s19
	s_mul_hi_u32 s19, s9, s24
	s_mul_i32 s24, s19, s6
	s_sub_i32 s9, s9, s24
	s_add_i32 s24, s19, 1
	s_sub_i32 s25, s9, s6
	s_cmp_ge_u32 s9, s6
	s_cselect_b32 s19, s24, s19
	s_cselect_b32 s9, s25, s9
	s_add_i32 s24, s19, 1
	s_cmp_ge_u32 s9, s6
	s_cselect_b32 s6, s24, s19
	s_xor_b32 s6, s6, s4
	s_sub_i32 s6, s6, s4
	s_sext_i32_i8 s4, s10
	v_cvt_f32_i32_e32 v11, s4
	s_mul_i32 s8, s6, s8
	s_sub_i32 s7, s7, s8
	v_cvt_f32_i32_e32 v28, s7
	v_rcp_iflag_f32_e32 v29, v11
	s_xor_b32 s4, s7, s4
	s_ashr_i32 s4, s4, 30
	s_or_b32 s4, s4, 1
	v_mul_f32_e32 v29, v28, v29
	v_trunc_f32_e32 v29, v29
	v_fma_f32 v28, -v29, v11, v28
	v_cvt_i32_f32_e32 v29, v29
	v_cmp_ge_f32_e64 s[8:9], |v28|, |v11|
	s_and_b64 s[8:9], s[8:9], exec
	s_cselect_b32 s4, s4, 0
	v_readfirstlane_b32 s8, v29
	s_add_i32 s8, s8, s4
	s_mul_i32 s9, s8, s10
	s_sub_i32 s10, s7, s9
	s_sext_i32_i8 s7, s10
	v_lshl_add_u32 v11, s7, 7, v12
	v_lshl_or_b32 v28, s7, 8, v13
	s_ashr_i32 s7, s6, 31
	s_sext_i32_i8 s4, s8
	s_lshl_b64 s[18:19], s[6:7], s18
	v_lshl_or_b32 v30, s4, 6, v14
	s_lshl_b64 s[18:19], s[18:19], 2
	v_ashrrev_i32_e32 v31, 31, v30
	s_add_u32 s18, s20, s18
	v_cndmask_b32_e32 v28, v11, v28, vcc
	s_addc_u32 s19, s17, s19
	v_lshlrev_b64 v[30:31], s21, v[30:31]
	v_lshl_add_u64 v[30:31], v[30:31], 2, s[18:19]
	v_ashrrev_i32_e32 v29, 31, v28
	v_lshl_add_u64 v[52:53], v[28:29], 2, v[30:31]
	s_lshl_b64 s[18:19], 12, s21
	s_lshl_b32 s4, s11, 2
	v_lshl_add_u64 v[40:41], v[52:53], 0, s[18:19]
	s_lshl_b64 s[18:19], 24, s21
	v_lshl_add_u64 v[36:37], v[52:53], 0, s[4:5]
	v_lshl_add_u64 v[44:45], v[52:53], 0, s[18:19]
	s_lshl_b64 s[18:19], 28, s21
	v_lshl_add_u64 v[54:55], v[36:37], 0, s[4:5]
	v_lshl_add_u64 v[48:49], v[52:53], 0, s[18:19]
	s_lshl_b32 s4, s11, 3
	s_lshl_b64 s[18:19], 20, s21
	global_load_dwordx4 v[28:31], v[52:53], off nt
	global_load_dwordx4 v[32:35], v[36:37], off nt
	s_nop 0
	global_load_dwordx4 v[36:39], v[54:55], off nt
	s_nop 0
	global_load_dwordx4 v[40:43], v[40:41], off nt
	v_lshl_add_u64 v[54:55], v[54:55], 0, s[4:5]
	v_lshl_add_u64 v[56:57], v[52:53], 0, s[18:19]
	global_load_dwordx4 v[44:47], v[44:45], off nt
	s_nop 0
	global_load_dwordx4 v[48:51], v[48:49], off nt
	s_nop 0
	global_load_dwordx4 v[52:55], v[54:55], off nt
	s_nop 0
	global_load_dwordx4 v[56:59], v[56:57], off nt
	s_lshl_b64 s[6:7], s[6:7], s21
	s_lshl_b64 s[6:7], s[6:7], 11
	s_add_u32 s4, s22, s6
	s_addc_u32 s11, s23, s7
	s_bfe_i64 s[6:7], s[10:11], 0x80000
	s_bfe_i64 s[8:9], s[8:9], 0x80000
	s_lshl_b64 s[6:7], s[6:7], 19
	s_add_u32 s4, s4, s6
	s_addc_u32 s10, s11, s7
	s_lshl_b64 s[6:7], s[8:9], 15
	s_add_u32 s6, s4, s6
	s_addc_u32 s7, s10, s7
	v_mov_b32_e32 v11, v3
	s_add_i32 s3, s3, -1
	s_cmp_eq_u32 s3, 0
	s_waitcnt vmcnt(7)
	ds_write_b128 v16, v[28:31]
	s_waitcnt vmcnt(6)
	ds_write2_b32 v17, v32, v33 offset1:1
	ds_write2_b32 v18, v34, v35 offset1:1
	s_waitcnt vmcnt(3)
	ds_write2_b64 v24, v[44:45], v[46:47] offset1:1
	s_waitcnt vmcnt(2)
	ds_write2_b32 v25, v48, v49 offset1:1
	ds_write2_b32 v26, v50, v51 offset1:1
	ds_write2_b64 v19, v[36:37], v[38:39] offset1:1
	ds_write2_b32 v20, v40, v41 offset1:1
	ds_write2_b32 v21, v42, v43 offset1:1
	s_waitcnt vmcnt(1)
	ds_write_b128 v16, v[52:55] offset:4112
	s_waitcnt vmcnt(0)
	ds_write2_b32 v22, v56, v57 offset1:1
	ds_write2_b32 v23, v58, v59 offset1:1
	s_waitcnt lgkmcnt(0)
	s_barrier
	ds_read_b32 v28, v27 offset:1028
	ds_read_b32 v29, v27 offset:3084
	ds_read_b32 v30, v27 offset:5140
	ds_read_b32 v31, v27 offset:7196
	ds_read_b32 v32, v27 offset:6168
	ds_read_b32 v33, v27 offset:4112
	ds_read_b32 v34, v27 offset:2056
	ds_read_b32 v35, v27
	s_waitcnt lgkmcnt(0)
	v_cvt_pk_bf16_f32 v28, v35, v28
	v_cvt_pk_bf16_f32 v29, v34, v29
	v_cvt_pk_bf16_f32 v30, v33, v30
	v_cvt_pk_bf16_f32 v31, v32, v31
	ds_read_b32 v36, v27 offset:1060
	ds_read_b32 v37, v27 offset:3116
	ds_read_b32 v38, v27 offset:5172
	ds_read_b32 v39, v27 offset:7228
	ds_read_b32 v40, v27 offset:6200
	ds_read_b32 v41, v27 offset:4144
	ds_read_b32 v42, v27 offset:2088
	ds_read_b32 v43, v27 offset:32
	v_lshl_add_u64 v[32:33], s[6:7], 0, v[2:3]
	v_lshl_add_u64 v[34:35], v[32:33], 0, v[10:11]
	global_store_dwordx4 v[34:35], v[28:31], off
	v_lshl_add_u64 v[34:35], v[4:5], 1, v[32:33]
	s_cselect_b64 s[6:7], -1, 0
	s_waitcnt lgkmcnt(0)
	v_cvt_pk_bf16_f32 v28, v43, v36
	v_cvt_pk_bf16_f32 v29, v42, v37
	v_cvt_pk_bf16_f32 v30, v41, v38
	v_cvt_pk_bf16_f32 v31, v40, v39
	ds_read_b32 v11, v27 offset:1092
	ds_read_b32 v36, v27 offset:3148
	ds_read_b32 v37, v27 offset:6232
	ds_read_b32 v38, v27 offset:4176
	ds_read_b32 v39, v27 offset:2120
	ds_read_b32 v40, v27 offset:64
	ds_read_b32 v41, v27 offset:5204
	ds_read_b32 v42, v27 offset:7260
	global_store_dwordx4 v[34:35], v[28:31], off
	v_lshl_add_u64 v[34:35], v[6:7], 1, v[32:33]
	v_lshl_add_u64 v[32:33], v[8:9], 1, v[32:33]
	s_waitcnt lgkmcnt(2)
	v_cvt_pk_bf16_f32 v28, v40, v11
	v_cvt_pk_bf16_f32 v29, v39, v36
	s_waitcnt lgkmcnt(1)
	v_cvt_pk_bf16_f32 v30, v38, v41
	s_waitcnt lgkmcnt(0)
	v_cvt_pk_bf16_f32 v31, v37, v42
	ds_read_b32 v11, v27 offset:1124
	ds_read_b32 v36, v27 offset:3180
	ds_read_b32 v37, v27 offset:6264
	ds_read_b32 v38, v27 offset:4208
	ds_read_b32 v39, v27 offset:2152
	ds_read_b32 v40, v27 offset:96
	ds_read_b32 v41, v27 offset:5236
	ds_read_b32 v42, v27 offset:7292
	global_store_dwordx4 v[34:35], v[28:31], off
	s_waitcnt lgkmcnt(2)
	s_nop 0
	v_cvt_pk_bf16_f32 v28, v40, v11
	v_cvt_pk_bf16_f32 v29, v39, v36
	s_waitcnt lgkmcnt(1)
	v_cvt_pk_bf16_f32 v30, v38, v41
	s_waitcnt lgkmcnt(0)
	v_cvt_pk_bf16_f32 v31, v37, v42
	global_store_dwordx4 v[32:33], v[28:31], off
	s_branch .LBB0_1288

; #define LAS __attribute__((address_space(3)))
; #define SEAM(k) do { if (IN(k) && IN((k) + 1)) xcd_barrier(bar); \
;         if (PROBE_MASK) { const unsigned long long t_ = __builtin_amdgcn_s_memrealtime(); if ((PROBE_MASK >> (k)) & 1u) pr_acc += t_ - pr_t0; pr_t0 = t_; } } while (0)
; __device__ __forceinline__ void convert_deferred(const Ptrs& P, unsigned char* lds, int quota) {
;     const int tid = threadIdx.x, wid = tid >> 6, lane = tid & 63;
;     float* tile = (float*)lds;
;     volatile __attribute__((address_space(3))) int* slot = (volatile __attribute__((address_space(3))) int*)((__attribute__((address_space(3))) unsigned char*)lds + 131072 + 320 + 11000);
;     unsigned* q = (unsigned*)(P.ws + WS_CTL) + CW_DEFQ;
;     for (int n = 0; n < quota; ++n) {
;         __syncthreads();
;         if (tid == 0) *slot = (int)atomicAdd(q, 1u);
;         __syncthreads();
;         const int t = *slot;
;         if (t >= DEF_GU + DEF_DN) break;
;         const bool gu = t < DEF_GU;
;         const float* src = gu ? P.in[34] : P.in[36]; bf16* dst = (bf16*)(P.ws + (gu ? WS_WGU : WS_WDN));
;         const int N = gu ? 2048 : 1024, ntn = N / 256, it = gu ? 2 * NE * 16 * 8 - DEF_GU + t : 2 * NE * 16 * 4 - DEF_DN + (t - DEF_GU);
; __global__ void __launch_bounds__(NT, 2) mega(Args args) {
;     ...
;     if (IN(9)) { g8::MoeOrder S{(const char*)(ws + WS_ACT), (const char*)(ws + WS_WDN) + (size_t)0 * NE * 1024 * 1024 * 2, nullptr, (size_t)1024 * 1024 * 2, 4, D, G, vcu, 0, nullptr};
;         S.init((const unsigned*)(ws + WS_CTL) + CW_CNT + 0 * 64, (LAS int*)(LDSP + MISC_OFF + 256)); g8::EpiMoe2 E{P, 0}; g8::gemm_phase<g8::EpiMoe2, g8::MoeOrder, false, true>(LDSP, D, D, S, E);
;         { const int rem_ = ((LAS int*)(LDSP + MISC_OFF + 256))[96] % G; if (rem_ != 0 && vcu >= rem_) convert_deferred(P, lds, 5); } } SEAM(9);
.LBB0_1609:
	s_abs_i32 s0, s62
	v_cvt_f32_u32_e32 v2, s0
	s_sub_i32 s5, 0, s0
	s_abs_i32 s4, s9
	s_ashr_i32 s3, s9, 31
	v_rcp_iflag_f32_e32 v2, v2
	s_mov_b32 s1, 0
	v_mul_f32_e32 v2, 0x4f7ffffe, v2
	v_cvt_u32_f32_e32 v2, v2
	s_nop 0
	v_readfirstlane_b32 s6, v2
	s_mul_i32 s5, s5, s6
	s_mul_hi_u32 s5, s6, s5
	s_add_i32 s6, s6, s5
	s_mul_hi_u32 s5, s4, s6
	s_mul_i32 s5, s5, s0
	s_sub_i32 s4, s4, s5
	s_sub_i32 s5, s4, s0
	s_cmp_ge_u32 s4, s0
	s_cselect_b32 s4, s5, s4
	s_sub_i32 s5, s4, s0
	s_cmp_ge_u32 s4, s0
	s_cselect_b32 s0, s5, s4
	s_xor_b32 s0, s0, s3
	s_sub_i32 s0, s0, s3
	s_cmp_eq_u32 s0, 0
	v_readlane_b32 s3, v254, 2
	s_cselect_b64 s[4:5], -1, 0
	s_cmp_lt_i32 s3, s0
	s_cselect_b64 s[6:7], -1, 0
	s_or_b64 s[4:5], s[4:5], s[6:7]
	s_and_b64 vcc, exec, s[4:5]
	s_cbranch_vccnz .LBB0_1619
	v_and_b32_e32 v2, 0x7c, v175
	v_lshlrev_b32_e32 v3, 5, v0
	s_movk_i32 s0, 0x400
	v_and_or_b32 v12, v3, s0, v2
	v_bfe_u32 v2, v0, 3, 3
	v_lshl_or_b32 v4, v1, 5, v2
	v_lshlrev_b32_e32 v2, 3, v0
	v_lshl_add_u32 v11, v182, 4, 0
	v_and_b32_e32 v2, 56, v2
	v_mul_u32_u24_e32 v16, 0x2020, v1
	v_mov_b32_e32 v3, 0
	v_lshl_add_u32 v27, v4, 2, 0
	v_mul_u32_u24_e32 v28, 0x404, v2
	v_lshlrev_b32_e32 v10, 6, v4
	s_add_i32 s10, 0, 0x22c38
	v_add_u32_e32 v16, v11, v16
	s_mov_b32 s3, 7
	v_and_b32_e32 v13, 0xfc, v175
	v_and_b32_e32 v14, 56, v173
	v_or_b32_e32 v4, 0x200, v10
	v_mov_b32_e32 v5, v3
	v_or_b32_e32 v6, 0x400, v10
	v_mov_b32_e32 v7, v3
	v_or_b32_e32 v8, 0x600, v10
	v_mov_b32_e32 v9, v3
	v_mov_b32_e32 v15, s10
	s_movk_i32 s11, 0xf3b
	s_movk_i32 s12, 0x800
	s_mov_b32 s13, 0x1104e000
	s_movk_i32 s14, 0xc4
	v_add_u32_e32 v17, 0x404, v16
	v_add_u32_e32 v18, 0x40c, v16
	v_add_u32_e32 v19, 0x808, v16
	v_add_u32_e32 v20, 0xc0c, v16
	v_add_u32_e32 v21, 0xc14, v16
	v_add_u32_e32 v22, 0x1414, v16
	v_add_u32_e32 v23, 0x141c, v16
	v_add_u32_e32 v24, 0x1818, v16
	v_add_u32_e32 v25, 0x1c1c, v16
	v_add_u32_e32 v26, 0x1c24, v16
	v_lshlrev_b32_e32 v2, 1, v2
	v_add_u32_e32 v27, v27, v28
	v_lshlrev_b32_e32 v10, 1, v10
	s_branch .LBB0_1612

; __device__ __forceinline__ unsigned g8_cvt_pk(float lo, float hi) { unsigned r; asm volatile("v_cvt_pk_bf16_f32 %0, %1, %2" : "=v"(r) : "v"(lo), "v"(hi)); return r; }
; __device__ __forceinline__ void convert_deferred(const Ptrs& P, unsigned char* lds, int quota) {
;     ...
;         __syncthreads();
;         if (tid == 0) *slot = (int)atomicAdd(q, 1u);
;         __syncthreads();
;         const int t = *slot;
;         if (t >= DEF_GU + DEF_DN) break;
;         const bool gu = t < DEF_GU;
;         const float* src = gu ? P.in[34] : P.in[36]; bf16* dst = (bf16*)(P.ws + (gu ? WS_WGU : WS_WDN));
;         const int N = gu ? 2048 : 1024, ntn = N / 256, it = gu ? 2 * NE * 16 * 8 - DEF_GU + t : 2 * NE * 16 * 4 - DEF_DN + (t - DEF_GU);
;         f32x4 cur[8];
;         bt_load(src, N, gu ? 1 : 0, it, ntn, cur);
; #pragma unroll
;         for (int i = 0; i < 8; ++i) { float* tp = tile + (wid * 8 + i) * 257 + lane * 4; tp[0] = cur[i][0]; tp[1] = cur[i][1]; tp[2] = cur[i][2]; tp[3] = cur[i][3]; }
;         __syncthreads();
;         const int per = 16 * ntn, z = it / per, r = it % per, kt = r / ntn, nt = r % ntn;
;         bf16* d = dst + (size_t)z * N * 1024 + (((size_t)nt * 16 + kt) << 14);
;         const int kc = lane & 7;
; #pragma unroll
;         for (int pss = 0; pss < 4; ++pss) {
;             const int nn = wid * 32 + pss * 8 + (lane >> 3); float f[8];
; #pragma unroll
;             for (int j = 0; j < 8; ++j) f[j] = tile[(kc * 8 + j) * 257 + nn];
;             u32x4 w; w.x = g8_cvt_pk(f[0], f[1]); w.y = g8_cvt_pk(f[2], f[3]); w.z = g8_cvt_pk(f[4], f[5]); w.w = g8_cvt_pk(f[6], f[7]);
;             *(u32x4*)(d + nn * 64 + kc * 8) = w;
;         }
.LBB0_1616:
	s_or_b64 exec, exec, s[4:5]
	s_waitcnt lgkmcnt(0)
	s_barrier
	ds_read_b32 v11, v15
	s_mov_b64 s[4:5], -1
	s_waitcnt lgkmcnt(0)
	v_cmp_lt_i32_e32 vcc, s11, v11
	v_readfirstlane_b32 s0, v11
	s_cbranch_vccnz .LBB0_1611
	s_cmpk_gt_i32 s0, 0xa27
	s_cselect_b64 vcc, -1, 0
	s_and_b64 s[4:5], vcc, exec
	s_cselect_b32 s4, s13, 0x104e000
	s_cselect_b32 s9, 0x400, s12
	s_cselect_b32 s15, s73, s69
	s_cselect_b32 s18, s72, s68
	s_cselect_b32 s5, s14, 0x15d8
	s_cselect_b32 s16, 20, 21
	s_cselect_b32 s19, 10, 11
	s_add_u32 s20, s78, s4
	s_addc_u32 s21, s79, 0
	s_lshr_b32 s6, s9, 4
	s_abs_i32 s4, s6
	v_cvt_f32_u32_e32 v11, s4
	s_sub_i32 s17, 0, s4
	s_add_i32 s5, s5, s0
	s_abs_i32 s7, s5
	v_rcp_iflag_f32_e32 v11, v11
	s_xor_b32 s0, s5, s6
	s_lshr_b32 s8, s9, 8
	s_ashr_i32 s0, s0, 31
	v_mul_f32_e32 v11, 0x4f7ffffe, v11
	v_cvt_u32_f32_e32 v11, v11
	s_nop 0
	v_readfirstlane_b32 s22, v11
	s_mul_i32 s17, s17, s22
	s_mul_hi_u32 s17, s22, s17
	s_add_i32 s22, s22, s17
	s_mul_hi_u32 s17, s7, s22
	s_mul_i32 s22, s17, s4
	s_sub_i32 s7, s7, s22
	s_add_i32 s22, s17, 1
	s_sub_i32 s23, s7, s4
	s_cmp_ge_u32 s7, s4
	s_cselect_b32 s17, s22, s17
	s_cselect_b32 s7, s23, s7
	s_add_i32 s22, s17, 1
	s_cmp_ge_u32 s7, s4
	s_cselect_b32 s4, s22, s17
	s_xor_b32 s4, s4, s0
	s_sub_i32 s4, s4, s0
	s_sext_i32_i8 s0, s8
	v_cvt_f32_i32_e32 v11, s0
	s_mul_i32 s6, s4, s6
	s_sub_i32 s5, s5, s6
	v_cvt_f32_i32_e32 v28, s5
	v_rcp_iflag_f32_e32 v29, v11
	s_xor_b32 s0, s5, s0
	s_ashr_i32 s0, s0, 30
	s_or_b32 s0, s0, 1
	v_mul_f32_e32 v29, v28, v29
	v_trunc_f32_e32 v29, v29
	v_fma_f32 v28, -v29, v11, v28
	v_cvt_i32_f32_e32 v29, v29
	v_cmp_ge_f32_e64 s[6:7], |v28|, |v11|
	s_and_b64 s[6:7], s[6:7], exec
	s_cselect_b32 s0, s0, 0
	v_readfirstlane_b32 s6, v29
	s_add_i32 s6, s6, s0
	s_mul_i32 s7, s6, s8
	s_sub_i32 s8, s5, s7
	s_sext_i32_i8 s5, s8
	v_lshl_add_u32 v11, s5, 7, v12
	v_lshl_or_b32 v28, s5, 8, v13
	s_ashr_i32 s5, s4, 31
	s_sext_i32_i8 s0, s6
	s_lshl_b64 s[16:17], s[4:5], s16
	v_lshl_or_b32 v30, s0, 6, v14
	s_lshl_b64 s[16:17], s[16:17], 2
	v_ashrrev_i32_e32 v31, 31, v30
	s_add_u32 s16, s18, s16
	v_cndmask_b32_e32 v28, v11, v28, vcc
	s_addc_u32 s17, s15, s17
	v_lshlrev_b64 v[30:31], s19, v[30:31]
	v_lshl_add_u64 v[30:31], v[30:31], 2, s[16:17]
	v_ashrrev_i32_e32 v29, 31, v28
	v_lshl_add_u64 v[52:53], v[28:29], 2, v[30:31]
	s_lshl_b64 s[16:17], 12, s19
	s_lshl_b32 s0, s9, 2
	v_lshl_add_u64 v[40:41], v[52:53], 0, s[16:17]
	s_lshl_b64 s[16:17], 24, s19
	v_lshl_add_u64 v[36:37], v[52:53], 0, s[0:1]
	v_lshl_add_u64 v[44:45], v[52:53], 0, s[16:17]
	s_lshl_b64 s[16:17], 28, s19
	v_lshl_add_u64 v[54:55], v[36:37], 0, s[0:1]
	v_lshl_add_u64 v[48:49], v[52:53], 0, s[16:17]
	s_lshl_b32 s0, s9, 3
	s_lshl_b64 s[16:17], 20, s19
	global_load_dwordx4 v[28:31], v[52:53], off nt
	global_load_dwordx4 v[32:35], v[36:37], off nt
	s_nop 0
	global_load_dwordx4 v[36:39], v[54:55], off nt
	s_nop 0
	global_load_dwordx4 v[40:43], v[40:41], off nt
	v_lshl_add_u64 v[54:55], v[54:55], 0, s[0:1]
	v_lshl_add_u64 v[56:57], v[52:53], 0, s[16:17]
	global_load_dwordx4 v[44:47], v[44:45], off nt
	s_nop 0
	global_load_dwordx4 v[48:51], v[48:49], off nt
	s_nop 0
	global_load_dwordx4 v[52:55], v[54:55], off nt
	s_nop 0
	global_load_dwordx4 v[56:59], v[56:57], off nt
	s_lshl_b64 s[4:5], s[4:5], s19
	s_lshl_b64 s[4:5], s[4:5], 11
	s_add_u32 s0, s20, s4
	s_addc_u32 s9, s21, s5
	s_bfe_i64 s[4:5], s[8:9], 0x80000
	s_bfe_i64 s[6:7], s[6:7], 0x80000
	s_lshl_b64 s[4:5], s[4:5], 19
	s_add_u32 s0, s0, s4
	s_addc_u32 s8, s9, s5
	s_lshl_b64 s[4:5], s[6:7], 15
	s_add_u32 s4, s0, s4
	s_addc_u32 s5, s8, s5
	v_mov_b32_e32 v11, v3
	s_add_i32 s3, s3, -1
	s_cmp_eq_u32 s3, 0
	s_waitcnt vmcnt(7)
	ds_write_b128 v16, v[28:31]
	s_waitcnt vmcnt(6)
	ds_write2_b32 v17, v32, v33 offset1:1
	ds_write2_b32 v18, v34, v35 offset1:1
	s_waitcnt vmcnt(3)
	ds_write2_b64 v24, v[44:45], v[46:47] offset1:1
	s_waitcnt vmcnt(2)
	ds_write2_b32 v25, v48, v49 offset1:1
	ds_write2_b32 v26, v50, v51 offset1:1
	ds_write2_b64 v19, v[36:37], v[38:39] offset1:1
	ds_write2_b32 v20, v40, v41 offset1:1
	ds_write2_b32 v21, v42, v43 offset1:1
	s_waitcnt vmcnt(1)
	ds_write_b128 v16, v[52:55] offset:4112
	s_waitcnt vmcnt(0)
	ds_write2_b32 v22, v56, v57 offset1:1
	ds_write2_b32 v23, v58, v59 offset1:1
	s_waitcnt lgkmcnt(0)
	s_barrier
	ds_read_b32 v28, v27 offset:1028
	ds_read_b32 v29, v27 offset:3084
	ds_read_b32 v30, v27 offset:5140
	ds_read_b32 v31, v27 offset:7196
	ds_read_b32 v32, v27 offset:6168
	ds_read_b32 v33, v27 offset:4112
	ds_read_b32 v34, v27 offset:2056
	ds_read_b32 v35, v27
	s_waitcnt lgkmcnt(0)
	v_cvt_pk_bf16_f32 v28, v35, v28
	v_cvt_pk_bf16_f32 v29, v34, v29
	v_cvt_pk_bf16_f32 v30, v33, v30
	v_cvt_pk_bf16_f32 v31, v32, v31
	ds_read_b32 v36, v27 offset:1060
	ds_read_b32 v37, v27 offset:3116
	ds_read_b32 v38, v27 offset:5172
	ds_read_b32 v39, v27 offset:7228
	ds_read_b32 v40, v27 offset:6200
	ds_read_b32 v41, v27 offset:4144
	ds_read_b32 v42, v27 offset:2088
	ds_read_b32 v43, v27 offset:32
	v_lshl_add_u64 v[32:33], s[4:5], 0, v[2:3]
	v_lshl_add_u64 v[34:35], v[32:33], 0, v[10:11]
	global_store_dwordx4 v[34:35], v[28:31], off
	v_lshl_add_u64 v[34:35], v[4:5], 1, v[32:33]
	s_cselect_b64 s[4:5], -1, 0
	s_waitcnt lgkmcnt(0)
	v_cvt_pk_bf16_f32 v28, v43, v36
	v_cvt_pk_bf16_f32 v29, v42, v37
	v_cvt_pk_bf16_f32 v30, v41, v38
	v_cvt_pk_bf16_f32 v31, v40, v39
	ds_read_b32 v11, v27 offset:1092
	ds_read_b32 v36, v27 offset:3148
	ds_read_b32 v37, v27 offset:6232
	ds_read_b32 v38, v27 offset:4176
	ds_read_b32 v39, v27 offset:2120
	ds_read_b32 v40, v27 offset:64
	ds_read_b32 v41, v27 offset:5204
	ds_read_b32 v42, v27 offset:7260
	global_store_dwordx4 v[34:35], v[28:31], off
	v_lshl_add_u64 v[34:35], v[6:7], 1, v[32:33]
	v_lshl_add_u64 v[32:33], v[8:9], 1, v[32:33]
	s_waitcnt lgkmcnt(2)
	v_cvt_pk_bf16_f32 v28, v40, v11
	v_cvt_pk_bf16_f32 v29, v39, v36
	s_waitcnt lgkmcnt(1)
	v_cvt_pk_bf16_f32 v30, v38, v41
	s_waitcnt lgkmcnt(0)
	v_cvt_pk_bf16_f32 v31, v37, v42
	ds_read_b32 v11, v27 offset:1124
	ds_read_b32 v36, v27 offset:3180
	ds_read_b32 v37, v27 offset:6264
	ds_read_b32 v38, v27 offset:4208
	ds_read_b32 v39, v27 offset:2152
	ds_read_b32 v40, v27 offset:96
	ds_read_b32 v41, v27 offset:5236
	ds_read_b32 v42, v27 offset:7292
	global_store_dwordx4 v[34:35], v[28:31], off
	s_waitcnt lgkmcnt(2)
	s_nop 0
	v_cvt_pk_bf16_f32 v28, v40, v11
	v_cvt_pk_bf16_f32 v29, v39, v36
	s_waitcnt lgkmcnt(1)
	v_cvt_pk_bf16_f32 v30, v38, v41
	s_waitcnt lgkmcnt(0)
	v_cvt_pk_bf16_f32 v31, v37, v42
	global_store_dwordx4 v[32:33], v[28:31], off
	s_branch .LBB0_1611

; #define LAS __attribute__((address_space(3)))
; #define SEAM(k) do { if (IN(k) && IN((k) + 1)) xcd_barrier(bar); \
;         if (PROBE_MASK) { const unsigned long long t_ = __builtin_amdgcn_s_memrealtime(); if ((PROBE_MASK >> (k)) & 1u) pr_acc += t_ - pr_t0; pr_t0 = t_; } } while (0)
; __device__ __forceinline__ void convert_deferred(const Ptrs& P, unsigned char* lds, int quota) {
;     const int tid = threadIdx.x, wid = tid >> 6, lane = tid & 63;
;     float* tile = (float*)lds;
;     volatile __attribute__((address_space(3))) int* slot = (volatile __attribute__((address_space(3))) int*)((__attribute__((address_space(3))) unsigned char*)lds + 131072 + 320 + 11000);
;     unsigned* q = (unsigned*)(P.ws + WS_CTL) + CW_DEFQ;
;     for (int n = 0; n < quota; ++n) {
;         __syncthreads();
;         if (tid == 0) *slot = (int)atomicAdd(q, 1u);
;         __syncthreads();
;         const int t = *slot;
;         if (t >= DEF_GU + DEF_DN) break;
;         const bool gu = t < DEF_GU;
;         const float* src = gu ? P.in[34] : P.in[36]; bf16* dst = (bf16*)(P.ws + (gu ? WS_WGU : WS_WDN));
;         const int N = gu ? 2048 : 1024, ntn = N / 256, it = gu ? 2 * NE * 16 * 8 - DEF_GU + t : 2 * NE * 16 * 4 - DEF_DN + (t - DEF_GU);
; __global__ void __launch_bounds__(NT, 2) mega(Args args) {
;     ...
;     if (IN(11)) { g8::DenseOrder S; S.init(H, D, (const bf16*)(ws + WS_WODIN), D, R, ODD_IN, G, (int)blockIdx.x, 0);
;         g8::EpiDiffIn E{Z, P.in[25], P.in[26], (const float*)(ws + WS_ROPE), (const float*)(ws + WS_ROPE) + SEQ * 64, (LAS float*)(LDSP + MISC_OFF + 1024)};
;         g8::gemm_phase<g8::EpiDiffIn, g8::DenseOrder, false, true>(LDSP, D, D, S, E);
;         if (IDLE_LAST(68 * 12)) convert_deferred(P, lds, 4); } SEAM(11);
.LBB0_1851:
	s_abs_i32 s0, s62
	v_cvt_f32_u32_e32 v2, s0
	s_sub_i32 s3, 0, s0
	v_readlane_b32 s56, v254, 40
	s_mov_b32 s1, 0
	v_rcp_iflag_f32_e32 v2, v2
	v_readlane_b32 s57, v254, 41
	v_mul_f32_e32 v2, 0x4f7ffffe, v2
	v_cvt_u32_f32_e32 v2, v2
	s_nop 0
	v_readfirstlane_b32 s4, v2
	s_mul_i32 s3, s3, s4
	s_mul_hi_u32 s3, s4, s3
	s_add_i32 s4, s4, s3
	s_mul_hi_u32 s3, s4, 0x330
	s_mul_i32 s3, s3, s0
	s_sub_i32 s3, 0x330, s3
	s_sub_i32 s4, s3, s0
	s_cmp_ge_u32 s3, s0
	s_cselect_b32 s3, s4, s3
	s_sub_i32 s4, s3, s0
	s_cmp_ge_u32 s3, s0
	s_cselect_b32 s0, s4, s3
	s_cmp_eq_u32 s0, 0
	s_cselect_b64 s[4:5], -1, 0
	s_cmp_lt_i32 s2, s0
	s_cselect_b64 s[6:7], -1, 0
	s_or_b64 s[4:5], s[4:5], s[6:7]
	s_and_b64 vcc, exec, s[4:5]
	s_cbranch_vccnz .LBB0_1861
	v_and_b32_e32 v2, 0x7c, v218
	v_lshlrev_b32_e32 v3, 5, v0
	s_movk_i32 s0, 0x400
	v_and_or_b32 v12, v3, s0, v2
	v_bfe_u32 v2, v0, 3, 3
	v_lshl_or_b32 v4, v1, 5, v2
	v_lshlrev_b32_e32 v2, 3, v0
	v_lshl_add_u32 v11, v182, 4, 0
	v_and_b32_e32 v2, 56, v2
	v_mul_u32_u24_e32 v16, 0x2020, v1
	v_mov_b32_e32 v3, 0
	s_waitcnt vmcnt(0)
	v_lshl_add_u32 v27, v4, 2, 0
	v_mul_u32_u24_e32 v28, 0x404, v2
	v_lshlrev_b32_e32 v10, 6, v4
	s_add_i32 s10, 0, 0x22c38
	v_add_u32_e32 v16, v11, v16
	v_and_b32_e32 v13, 0xfc, v218
	v_and_b32_e32 v14, 56, v179
	s_mov_b32 s3, 8
	v_or_b32_e32 v4, 0x200, v10
	v_mov_b32_e32 v5, v3
	v_or_b32_e32 v6, 0x400, v10
	v_mov_b32_e32 v7, v3
	v_or_b32_e32 v8, 0x600, v10
	v_mov_b32_e32 v9, v3
	v_mov_b32_e32 v15, s10
	s_movk_i32 s11, 0xf3b
	s_movk_i32 s12, 0x800
	s_mov_b32 s13, 0x1104e000
	s_movk_i32 s14, 0xc4
	v_add_u32_e32 v17, 0x404, v16
	v_add_u32_e32 v18, 0x40c, v16
	v_add_u32_e32 v19, 0x808, v16
	v_add_u32_e32 v20, 0xc0c, v16
	v_add_u32_e32 v21, 0xc14, v16
	v_add_u32_e32 v22, 0x1414, v16
	v_add_u32_e32 v23, 0x141c, v16
	v_add_u32_e32 v24, 0x1818, v16
	v_add_u32_e32 v25, 0x1c1c, v16
	v_add_u32_e32 v26, 0x1c24, v16
	v_lshlrev_b32_e32 v2, 1, v2
	v_add_u32_e32 v27, v27, v28
	v_lshlrev_b32_e32 v10, 1, v10
	s_branch .LBB0_1854

; __device__ __forceinline__ unsigned g8_cvt_pk(float lo, float hi) { unsigned r; asm volatile("v_cvt_pk_bf16_f32 %0, %1, %2" : "=v"(r) : "v"(lo), "v"(hi)); return r; }
; __device__ __forceinline__ void convert_deferred(const Ptrs& P, unsigned char* lds, int quota) {
;     ...
;         __syncthreads();
;         if (tid == 0) *slot = (int)atomicAdd(q, 1u);
;         __syncthreads();
;         const int t = *slot;
;         if (t >= DEF_GU + DEF_DN) break;
;         const bool gu = t < DEF_GU;
;         const float* src = gu ? P.in[34] : P.in[36]; bf16* dst = (bf16*)(P.ws + (gu ? WS_WGU : WS_WDN));
;         const int N = gu ? 2048 : 1024, ntn = N / 256, it = gu ? 2 * NE * 16 * 8 - DEF_GU + t : 2 * NE * 16 * 4 - DEF_DN + (t - DEF_GU);
;         f32x4 cur[8];
;         bt_load(src, N, gu ? 1 : 0, it, ntn, cur);
; #pragma unroll
;         for (int i = 0; i < 8; ++i) { float* tp = tile + (wid * 8 + i) * 257 + lane * 4; tp[0] = cur[i][0]; tp[1] = cur[i][1]; tp[2] = cur[i][2]; tp[3] = cur[i][3]; }
;         __syncthreads();
;         const int per = 16 * ntn, z = it / per, r = it % per, kt = r / ntn, nt = r % ntn;
;         bf16* d = dst + (size_t)z * N * 1024 + (((size_t)nt * 16 + kt) << 14);
;         const int kc = lane & 7;
; #pragma unroll
;         for (int pss = 0; pss < 4; ++pss) {
;             const int nn = wid * 32 + pss * 8 + (lane >> 3); float f[8];
; #pragma unroll
;             for (int j = 0; j < 8; ++j) f[j] = tile[(kc * 8 + j) * 257 + nn];
;             u32x4 w; w.x = g8_cvt_pk(f[0], f[1]); w.y = g8_cvt_pk(f[2], f[3]); w.z = g8_cvt_pk(f[4], f[5]); w.w = g8_cvt_pk(f[6], f[7]);
;             *(u32x4*)(d + nn * 64 + kc * 8) = w;
;         }
.LBB0_1858:
	s_or_b64 exec, exec, s[4:5]
	s_waitcnt lgkmcnt(0)
	s_barrier
	ds_read_b32 v11, v15
	s_mov_b64 s[4:5], -1
	s_waitcnt lgkmcnt(0)
	v_cmp_lt_i32_e32 vcc, s11, v11
	v_readfirstlane_b32 s0, v11
	s_cbranch_vccnz .LBB0_1853
	s_cmpk_gt_i32 s0, 0xa27
	s_cselect_b64 vcc, -1, 0
	s_and_b64 s[4:5], vcc, exec
	s_cselect_b32 s4, s13, 0x104e000
	s_cselect_b32 s9, 0x400, s12
	s_cselect_b32 s15, s73, s69
	s_cselect_b32 s20, s72, s68
	s_cselect_b32 s5, s14, 0x15d8
	s_cselect_b32 s16, 20, 21
	s_cselect_b32 s21, 10, 11
	s_add_u32 s22, s78, s4
	s_addc_u32 s23, s79, 0
	s_lshr_b32 s6, s9, 4
	s_abs_i32 s4, s6
	v_cvt_f32_u32_e32 v11, s4
	s_sub_i32 s17, 0, s4
	s_add_i32 s5, s5, s0
	s_abs_i32 s7, s5
	v_rcp_iflag_f32_e32 v11, v11
	s_xor_b32 s0, s5, s6
	s_lshr_b32 s8, s9, 8
	s_ashr_i32 s0, s0, 31
	v_mul_f32_e32 v11, 0x4f7ffffe, v11
	v_cvt_u32_f32_e32 v11, v11
	s_nop 0
	v_readfirstlane_b32 s24, v11
	s_mul_i32 s17, s17, s24
	s_mul_hi_u32 s17, s24, s17
	s_add_i32 s24, s24, s17
	s_mul_hi_u32 s17, s7, s24
	s_mul_i32 s24, s17, s4
	s_sub_i32 s7, s7, s24
	s_add_i32 s24, s17, 1
	s_sub_i32 s25, s7, s4
	s_cmp_ge_u32 s7, s4
	s_cselect_b32 s17, s24, s17
	s_cselect_b32 s7, s25, s7
	s_add_i32 s24, s17, 1
	s_cmp_ge_u32 s7, s4
	s_cselect_b32 s4, s24, s17
	s_xor_b32 s4, s4, s0
	s_sub_i32 s4, s4, s0
	s_sext_i32_i8 s0, s8
	v_cvt_f32_i32_e32 v11, s0
	s_mul_i32 s6, s4, s6
	s_sub_i32 s5, s5, s6
	v_cvt_f32_i32_e32 v28, s5
	v_rcp_iflag_f32_e32 v29, v11
	s_xor_b32 s0, s5, s0
	s_ashr_i32 s0, s0, 30
	s_or_b32 s0, s0, 1
	v_mul_f32_e32 v29, v28, v29
	v_trunc_f32_e32 v29, v29
	v_fma_f32 v28, -v29, v11, v28
	v_cvt_i32_f32_e32 v29, v29
	v_cmp_ge_f32_e64 s[6:7], |v28|, |v11|
	s_and_b64 s[6:7], s[6:7], exec
	s_cselect_b32 s0, s0, 0
	v_readfirstlane_b32 s6, v29
	s_add_i32 s6, s6, s0
	s_mul_i32 s7, s6, s8
	s_sub_i32 s8, s5, s7
	s_sext_i32_i8 s5, s8
	v_lshl_add_u32 v11, s5, 7, v12
	v_lshl_or_b32 v28, s5, 8, v13
	s_ashr_i32 s5, s4, 31
	s_sext_i32_i8 s0, s6
	s_lshl_b64 s[16:17], s[4:5], s16
	v_lshl_or_b32 v30, s0, 6, v14
	s_lshl_b64 s[16:17], s[16:17], 2
	v_ashrrev_i32_e32 v31, 31, v30
	s_add_u32 s16, s20, s16
	v_cndmask_b32_e32 v28, v11, v28, vcc
	s_addc_u32 s17, s15, s17
	v_lshlrev_b64 v[30:31], s21, v[30:31]
	v_lshl_add_u64 v[30:31], v[30:31], 2, s[16:17]
	v_ashrrev_i32_e32 v29, 31, v28
	v_lshl_add_u64 v[52:53], v[28:29], 2, v[30:31]
	s_lshl_b64 s[16:17], 12, s21
	s_lshl_b32 s0, s9, 2
	v_lshl_add_u64 v[40:41], v[52:53], 0, s[16:17]
	s_lshl_b64 s[16:17], 24, s21
	v_lshl_add_u64 v[36:37], v[52:53], 0, s[0:1]
	v_lshl_add_u64 v[44:45], v[52:53], 0, s[16:17]
	s_lshl_b64 s[16:17], 28, s21
	v_lshl_add_u64 v[54:55], v[36:37], 0, s[0:1]
	v_lshl_add_u64 v[48:49], v[52:53], 0, s[16:17]
	s_lshl_b32 s0, s9, 3
	s_lshl_b64 s[16:17], 20, s21
	global_load_dwordx4 v[28:31], v[52:53], off nt
	global_load_dwordx4 v[32:35], v[36:37], off nt
	s_nop 0
	global_load_dwordx4 v[36:39], v[54:55], off nt
	s_nop 0
	global_load_dwordx4 v[40:43], v[40:41], off nt
	v_lshl_add_u64 v[54:55], v[54:55], 0, s[0:1]
	v_lshl_add_u64 v[56:57], v[52:53], 0, s[16:17]
	global_load_dwordx4 v[44:47], v[44:45], off nt
	s_nop 0
	global_load_dwordx4 v[48:51], v[48:49], off nt
	s_nop 0
	global_load_dwordx4 v[52:55], v[54:55], off nt
	s_nop 0
	global_load_dwordx4 v[56:59], v[56:57], off nt
	s_lshl_b64 s[4:5], s[4:5], s21
	s_lshl_b64 s[4:5], s[4:5], 11
	s_add_u32 s0, s22, s4
	s_addc_u32 s9, s23, s5
	s_bfe_i64 s[4:5], s[8:9], 0x80000
	s_bfe_i64 s[6:7], s[6:7], 0x80000
	s_lshl_b64 s[4:5], s[4:5], 19
	s_add_u32 s0, s0, s4
	s_addc_u32 s8, s9, s5
	s_lshl_b64 s[4:5], s[6:7], 15
	s_add_u32 s4, s0, s4
	s_addc_u32 s5, s8, s5
	v_mov_b32_e32 v11, v3
	s_add_i32 s3, s3, -1
	s_cmp_eq_u32 s3, 0
	s_waitcnt vmcnt(7)
	ds_write_b128 v16, v[28:31]
	s_waitcnt vmcnt(6)
	ds_write2_b32 v17, v32, v33 offset1:1
	ds_write2_b32 v18, v34, v35 offset1:1
	s_waitcnt vmcnt(3)
	ds_write2_b64 v24, v[44:45], v[46:47] offset1:1
	s_waitcnt vmcnt(2)
	ds_write2_b32 v25, v48, v49 offset1:1
	ds_write2_b32 v26, v50, v51 offset1:1
	ds_write2_b64 v19, v[36:37], v[38:39] offset1:1
	ds_write2_b32 v20, v40, v41 offset1:1
	ds_write2_b32 v21, v42, v43 offset1:1
	s_waitcnt vmcnt(1)
	ds_write_b128 v16, v[52:55] offset:4112
	s_waitcnt vmcnt(0)
	ds_write2_b32 v22, v56, v57 offset1:1
	ds_write2_b32 v23, v58, v59 offset1:1
	s_waitcnt lgkmcnt(0)
	s_barrier
	ds_read_b32 v28, v27 offset:1028
	ds_read_b32 v29, v27 offset:3084
	ds_read_b32 v30, v27 offset:5140
	ds_read_b32 v31, v27 offset:7196
	ds_read_b32 v32, v27 offset:6168
	ds_read_b32 v33, v27 offset:4112
	ds_read_b32 v34, v27 offset:2056
	ds_read_b32 v35, v27
	s_waitcnt lgkmcnt(0)
	v_cvt_pk_bf16_f32 v28, v35, v28
	v_cvt_pk_bf16_f32 v29, v34, v29
	v_cvt_pk_bf16_f32 v30, v33, v30
	v_cvt_pk_bf16_f32 v31, v32, v31
	ds_read_b32 v36, v27 offset:1060
	ds_read_b32 v37, v27 offset:3116
	ds_read_b32 v38, v27 offset:5172
	ds_read_b32 v39, v27 offset:7228
	ds_read_b32 v40, v27 offset:6200
	ds_read_b32 v41, v27 offset:4144
	ds_read_b32 v42, v27 offset:2088
	ds_read_b32 v43, v27 offset:32
	v_lshl_add_u64 v[32:33], s[4:5], 0, v[2:3]
	v_lshl_add_u64 v[34:35], v[32:33], 0, v[10:11]
	global_store_dwordx4 v[34:35], v[28:31], off
	v_lshl_add_u64 v[34:35], v[4:5], 1, v[32:33]
	s_cselect_b64 s[4:5], -1, 0
	s_waitcnt lgkmcnt(0)
	v_cvt_pk_bf16_f32 v28, v43, v36
	v_cvt_pk_bf16_f32 v29, v42, v37
	v_cvt_pk_bf16_f32 v30, v41, v38
	v_cvt_pk_bf16_f32 v31, v40, v39
	ds_read_b32 v11, v27 offset:1092
	ds_read_b32 v36, v27 offset:3148
	ds_read_b32 v37, v27 offset:6232
	ds_read_b32 v38, v27 offset:4176
	ds_read_b32 v39, v27 offset:2120
	ds_read_b32 v40, v27 offset:64
	ds_read_b32 v41, v27 offset:5204
	ds_read_b32 v42, v27 offset:7260
	global_store_dwordx4 v[34:35], v[28:31], off
	v_lshl_add_u64 v[34:35], v[6:7], 1, v[32:33]
	v_lshl_add_u64 v[32:33], v[8:9], 1, v[32:33]
	s_waitcnt lgkmcnt(2)
	v_cvt_pk_bf16_f32 v28, v40, v11
	v_cvt_pk_bf16_f32 v29, v39, v36
	s_waitcnt lgkmcnt(1)
	v_cvt_pk_bf16_f32 v30, v38, v41
	s_waitcnt lgkmcnt(0)
	v_cvt_pk_bf16_f32 v31, v37, v42
	ds_read_b32 v11, v27 offset:1124
	ds_read_b32 v36, v27 offset:3180
	ds_read_b32 v37, v27 offset:6264
	ds_read_b32 v38, v27 offset:4208
	ds_read_b32 v39, v27 offset:2152
	ds_read_b32 v40, v27 offset:96
	ds_read_b32 v41, v27 offset:5236
	ds_read_b32 v42, v27 offset:7292
	global_store_dwordx4 v[34:35], v[28:31], off
	s_waitcnt lgkmcnt(2)
	s_nop 0
	v_cvt_pk_bf16_f32 v28, v40, v11
	v_cvt_pk_bf16_f32 v29, v39, v36
	s_waitcnt lgkmcnt(1)
	v_cvt_pk_bf16_f32 v30, v38, v41
	s_waitcnt lgkmcnt(0)
	v_cvt_pk_bf16_f32 v31, v37, v42
	global_store_dwordx4 v[32:33], v[28:31], off
	s_branch .LBB0_1853

; #define SEAM(k) do { if (IN(k) && IN((k) + 1)) xcd_barrier(bar); \
;         if (PROBE_MASK) { const unsigned long long t_ = __builtin_amdgcn_s_memrealtime(); if ((PROBE_MASK >> (k)) & 1u) pr_acc += t_ - pr_t0; pr_t0 = t_; } } while (0)
; __device__ __forceinline__ void convert_deferred(const Ptrs& P, unsigned char* lds, int quota) {
;     const int tid = threadIdx.x, wid = tid >> 6, lane = tid & 63;
;     float* tile = (float*)lds;
;     volatile __attribute__((address_space(3))) int* slot = (volatile __attribute__((address_space(3))) int*)((__attribute__((address_space(3))) unsigned char*)lds + 131072 + 320 + 11000);
;     unsigned* q = (unsigned*)(P.ws + WS_CTL) + CW_DEFQ;
;     for (int n = 0; n < quota; ++n) {
;         __syncthreads();
;         if (tid == 0) *slot = (int)atomicAdd(q, 1u);
;         __syncthreads();
;         const int t = *slot;
;         if (t >= DEF_GU + DEF_DN) break;
;         const bool gu = t < DEF_GU;
;         const float* src = gu ? P.in[34] : P.in[36]; bf16* dst = (bf16*)(P.ws + (gu ? WS_WGU : WS_WDN));
;         const int N = gu ? 2048 : 1024, ntn = N / 256, it = gu ? 2 * NE * 16 * 8 - DEF_GU + t : 2 * NE * 16 * 4 - DEF_DN + (t - DEF_GU);
; __global__ void __launch_bounds__(NT, 2) mega(Args args) {
;     ...
;     if (IN(15)) { ph_norm2_router(P, lds, 1, 1); convert_deferred(P, lds, 1 << 20); } SEAM(15);
.LBB0_2278:
	v_and_b32_e32 v2, 0x7c, v179
	v_lshlrev_b32_e32 v3, 5, v0
	s_movk_i32 s0, 0x400
	v_and_or_b32 v12, v3, s0, v2
	v_lshrrev_b32_e32 v2, 3, v0
	v_and_b32_e32 v14, 56, v2
	v_lshrrev_b32_e32 v2, 3, v182
	v_lshl_or_b32 v4, v1, 5, v2
	v_lshl_add_u32 v5, v182, 4, 0
	v_and_b32_e32 v2, 56, v188
	v_lshl_add_u32 v7, v4, 2, 0
	v_mul_u32_u24_e32 v11, 0x2020, v1
	v_lshlrev_b32_e32 v4, 6, v4
	v_mul_u32_u24_e32 v9, 0x404, v2
	v_or_b32_e32 v6, 0x200, v4
	v_or_b32_e32 v8, 0x400, v4
	v_or_b32_e32 v10, 0x600, v4
	s_add_i32 s10, 0, 0x22c38
	v_add_u32_e32 v16, v5, v11
	v_and_b32_e32 v13, 0xfc, v179
	s_mov_b32 s1, 0
	v_mov_b32_e32 v3, 0
	s_mov_b32 s3, 0x100000
	v_mov_b32_e32 v15, s10
	s_movk_i32 s11, 0xf3b
	s_movk_i32 s12, 0x800
	s_mov_b32 s13, 0x1104e000
	s_movk_i32 s14, 0xc4
	v_add_u32_e32 v17, 0x404, v16
	v_add_u32_e32 v18, 0x40c, v16
	v_add_u32_e32 v19, 0x808, v16
	v_add_u32_e32 v20, 0xc0c, v16
	v_add_u32_e32 v21, 0xc14, v16
	v_add_u32_e32 v22, 0x1414, v16
	v_add_u32_e32 v23, 0x141c, v16
	v_add_u32_e32 v24, 0x1818, v16
	v_add_u32_e32 v25, 0x1c1c, v16
	v_add_u32_e32 v26, 0x1c24, v16
	v_lshlrev_b32_e32 v2, 1, v2
	v_add_u32_e32 v27, v7, v9
	v_lshlrev_b32_e32 v4, 1, v4
	v_lshlrev_b32_e32 v6, 1, v6
	v_lshlrev_b32_e32 v8, 1, v8
	v_lshlrev_b32_e32 v10, 1, v10
	s_branch .LBB0_2280

; __device__ __forceinline__ unsigned g8_cvt_pk(float lo, float hi) { unsigned r; asm volatile("v_cvt_pk_bf16_f32 %0, %1, %2" : "=v"(r) : "v"(lo), "v"(hi)); return r; }
; __device__ __forceinline__ void convert_deferred(const Ptrs& P, unsigned char* lds, int quota) {
;     ...
;         __syncthreads();
;         if (tid == 0) *slot = (int)atomicAdd(q, 1u);
;         __syncthreads();
;         const int t = *slot;
;         if (t >= DEF_GU + DEF_DN) break;
;         const bool gu = t < DEF_GU;
;         const float* src = gu ? P.in[34] : P.in[36]; bf16* dst = (bf16*)(P.ws + (gu ? WS_WGU : WS_WDN));
;         const int N = gu ? 2048 : 1024, ntn = N / 256, it = gu ? 2 * NE * 16 * 8 - DEF_GU + t : 2 * NE * 16 * 4 - DEF_DN + (t - DEF_GU);
;         f32x4 cur[8];
;         bt_load(src, N, gu ? 1 : 0, it, ntn, cur);
; #pragma unroll
;         for (int i = 0; i < 8; ++i) { float* tp = tile + (wid * 8 + i) * 257 + lane * 4; tp[0] = cur[i][0]; tp[1] = cur[i][1]; tp[2] = cur[i][2]; tp[3] = cur[i][3]; }
;         __syncthreads();
;         const int per = 16 * ntn, z = it / per, r = it % per, kt = r / ntn, nt = r % ntn;
;         bf16* d = dst + (size_t)z * N * 1024 + (((size_t)nt * 16 + kt) << 14);
;         const int kc = lane & 7;
; #pragma unroll
;         for (int pss = 0; pss < 4; ++pss) {
;             const int nn = wid * 32 + pss * 8 + (lane >> 3); float f[8];
; #pragma unroll
;             for (int j = 0; j < 8; ++j) f[j] = tile[(kc * 8 + j) * 257 + nn];
;             u32x4 w; w.x = g8_cvt_pk(f[0], f[1]); w.y = g8_cvt_pk(f[2], f[3]); w.z = g8_cvt_pk(f[4], f[5]); w.w = g8_cvt_pk(f[6], f[7]);
;             *(u32x4*)(d + nn * 64 + kc * 8) = w;
;         }
.LBB0_2284:
	s_or_b64 exec, exec, s[4:5]
	s_waitcnt lgkmcnt(0)
	s_barrier
	ds_read_b32 v5, v15
	s_mov_b64 s[4:5], -1
	s_waitcnt lgkmcnt(0)
	v_cmp_lt_i32_e32 vcc, s11, v5
	v_readfirstlane_b32 s0, v5
	s_cbranch_vccnz .LBB0_2279
	s_cmpk_gt_i32 s0, 0xa27
	s_cselect_b64 vcc, -1, 0
	s_and_b64 s[4:5], vcc, exec
	s_cselect_b32 s4, s13, 0x104e000
	s_cselect_b32 s9, 0x400, s12
	s_cselect_b32 s15, s73, s69
	s_cselect_b32 s18, s72, s68
	s_cselect_b32 s5, s14, 0x15d8
	s_cselect_b32 s16, 20, 21
	s_cselect_b32 s19, 10, 11
	s_add_u32 s22, s78, s4
	s_addc_u32 s23, s79, 0
	s_lshr_b32 s6, s9, 4
	s_abs_i32 s4, s6
	v_cvt_f32_u32_e32 v5, s4
	s_sub_i32 s17, 0, s4
	s_add_i32 s5, s5, s0
	s_abs_i32 s7, s5
	v_rcp_iflag_f32_e32 v5, v5
	s_xor_b32 s0, s5, s6
	s_lshr_b32 s8, s9, 8
	s_ashr_i32 s0, s0, 31
	v_mul_f32_e32 v5, 0x4f7ffffe, v5
	v_cvt_u32_f32_e32 v5, v5
	s_nop 0
	v_readfirstlane_b32 s24, v5
	s_mul_i32 s17, s17, s24
	s_mul_hi_u32 s17, s24, s17
	s_add_i32 s24, s24, s17
	s_mul_hi_u32 s17, s7, s24
	s_mul_i32 s24, s17, s4
	s_sub_i32 s7, s7, s24
	s_add_i32 s24, s17, 1
	s_sub_i32 s25, s7, s4
	s_cmp_ge_u32 s7, s4
	s_cselect_b32 s17, s24, s17
	s_cselect_b32 s7, s25, s7
	s_add_i32 s24, s17, 1
	s_cmp_ge_u32 s7, s4
	s_cselect_b32 s4, s24, s17
	s_xor_b32 s4, s4, s0
	s_sub_i32 s4, s4, s0
	s_sext_i32_i8 s0, s8
	v_cvt_f32_i32_e32 v5, s0
	s_mul_i32 s6, s4, s6
	s_sub_i32 s5, s5, s6
	v_cvt_f32_i32_e32 v7, s5
	v_rcp_iflag_f32_e32 v9, v5
	s_xor_b32 s0, s5, s0
	s_ashr_i32 s0, s0, 30
	s_or_b32 s0, s0, 1
	v_mul_f32_e32 v9, v7, v9
	v_trunc_f32_e32 v9, v9
	v_fma_f32 v7, -v9, v5, v7
	v_cvt_i32_f32_e32 v9, v9
	v_cmp_ge_f32_e64 s[6:7], |v7|, |v5|
	s_and_b64 s[6:7], s[6:7], exec
	s_cselect_b32 s0, s0, 0
	v_readfirstlane_b32 s6, v9
	s_add_i32 s6, s6, s0
	s_mul_i32 s7, s6, s8
	s_sub_i32 s8, s5, s7
	s_sext_i32_i8 s5, s8
	v_lshl_add_u32 v5, s5, 7, v12
	v_lshl_or_b32 v7, s5, 8, v13
	s_ashr_i32 s5, s4, 31
	s_sext_i32_i8 s0, s6
	s_lshl_b64 s[16:17], s[4:5], s16
	v_lshl_or_b32 v30, s0, 6, v14
	s_lshl_b64 s[16:17], s[16:17], 2
	v_ashrrev_i32_e32 v31, 31, v30
	s_add_u32 s16, s18, s16
	v_cndmask_b32_e32 v28, v5, v7, vcc
	s_addc_u32 s17, s15, s17
	v_lshlrev_b64 v[30:31], s19, v[30:31]
	v_lshl_add_u64 v[30:31], v[30:31], 2, s[16:17]
	v_ashrrev_i32_e32 v29, 31, v28
	v_lshl_add_u64 v[52:53], v[28:29], 2, v[30:31]
	s_lshl_b32 s0, s9, 2
	s_lshl_b64 s[16:17], 12, s19
	v_lshl_add_u64 v[36:37], v[52:53], 0, s[0:1]
	v_lshl_add_u64 v[44:45], v[52:53], 0, s[16:17]
	s_lshl_b64 s[16:17], 24, s19
	v_lshl_add_u64 v[54:55], v[36:37], 0, s[0:1]
	v_lshl_add_u64 v[56:57], v[52:53], 0, s[16:17]
	s_lshl_b64 s[16:17], 28, s19
	s_lshl_b32 s0, s9, 3
	v_lshl_add_u64 v[58:59], v[52:53], 0, s[16:17]
	v_lshl_add_u64 v[60:61], v[54:55], 0, s[0:1]
	s_lshl_b64 s[16:17], 20, s19
	global_load_dwordx4 v[28:31], v[52:53], off nt
	global_load_dwordx4 v[32:35], v[36:37], off nt
	s_nop 0
	global_load_dwordx4 v[36:39], v[54:55], off nt
	global_load_dwordx4 v[40:43], v[44:45], off nt
	s_nop 0
	global_load_dwordx4 v[44:47], v[56:57], off nt
	global_load_dwordx4 v[48:51], v[58:59], off nt
	v_lshl_add_u64 v[62:63], v[52:53], 0, s[16:17]
	global_load_dwordx4 v[52:55], v[60:61], off nt
	global_load_dwordx4 v[56:59], v[62:63], off nt
	s_lshl_b64 s[4:5], s[4:5], s19
	s_lshl_b64 s[4:5], s[4:5], 11
	s_add_u32 s0, s22, s4
	s_addc_u32 s9, s23, s5
	s_bfe_i64 s[4:5], s[8:9], 0x80000
	s_bfe_i64 s[6:7], s[6:7], 0x80000
	s_lshl_b64 s[4:5], s[4:5], 19
	s_add_u32 s0, s0, s4
	s_addc_u32 s8, s9, s5
	s_lshl_b64 s[4:5], s[6:7], 15
	s_add_u32 s4, s0, s4
	s_addc_u32 s5, s8, s5
	v_mov_b32_e32 v5, v3
	s_add_i32 s3, s3, -1
	s_cmp_eq_u32 s3, 0
	s_waitcnt vmcnt(7)
	ds_write_b128 v16, v[28:31]
	s_waitcnt vmcnt(6)
	ds_write2_b32 v17, v32, v33 offset1:1
	ds_write2_b32 v18, v34, v35 offset1:1
	s_waitcnt vmcnt(3)
	ds_write2_b64 v24, v[44:45], v[46:47] offset1:1
	s_waitcnt vmcnt(2)
	ds_write2_b32 v25, v48, v49 offset1:1
	ds_write2_b32 v26, v50, v51 offset1:1
	ds_write2_b64 v19, v[36:37], v[38:39] offset1:1
	ds_write2_b32 v20, v40, v41 offset1:1
	ds_write2_b32 v21, v42, v43 offset1:1
	s_waitcnt vmcnt(1)
	ds_write_b128 v16, v[52:55] offset:4112
	s_waitcnt vmcnt(0)
	ds_write2_b32 v22, v56, v57 offset1:1
	ds_write2_b32 v23, v58, v59 offset1:1
	s_waitcnt lgkmcnt(0)
	s_barrier
	ds_read_b32 v7, v27 offset:1028
	ds_read_b32 v9, v27 offset:3084
	ds_read_b32 v11, v27 offset:5140
	ds_read_b32 v31, v27 offset:7196
	ds_read_b32 v32, v27 offset:6168
	ds_read_b32 v30, v27 offset:4112
	ds_read_b32 v29, v27 offset:2056
	ds_read_b32 v28, v27
	s_waitcnt lgkmcnt(0)
	v_cvt_pk_bf16_f32 v28, v28, v7
	v_cvt_pk_bf16_f32 v29, v29, v9
	v_cvt_pk_bf16_f32 v30, v30, v11
	v_cvt_pk_bf16_f32 v31, v32, v31
	ds_read_b32 v7, v27 offset:1060
	ds_read_b32 v9, v27 offset:3116
	ds_read_b32 v11, v27 offset:5172
	ds_read_b32 v36, v27 offset:7228
	ds_read_b32 v37, v27 offset:6200
	ds_read_b32 v38, v27 offset:4144
	ds_read_b32 v39, v27 offset:2088
	ds_read_b32 v40, v27 offset:32
	v_lshl_add_u64 v[32:33], s[4:5], 0, v[2:3]
	v_lshl_add_u64 v[34:35], v[32:33], 0, v[4:5]
	global_store_dwordx4 v[34:35], v[28:31], off
	s_cselect_b64 s[4:5], -1, 0
	s_waitcnt lgkmcnt(0)
	v_cvt_pk_bf16_f32 v28, v40, v7
	v_cvt_pk_bf16_f32 v29, v39, v9
	v_cvt_pk_bf16_f32 v30, v38, v11
	v_cvt_pk_bf16_f32 v31, v37, v36
	ds_read_b32 v5, v27 offset:1092
	ds_read_b32 v9, v27 offset:3148
	ds_read_b32 v11, v27 offset:5204
	ds_read_b32 v36, v27 offset:6232
	ds_read_b32 v37, v27 offset:4176
	ds_read_b32 v38, v27 offset:2120
	ds_read_b32 v39, v27 offset:64
	ds_read_b32 v40, v27 offset:7260
	v_mov_b32_e32 v7, v3
	v_lshl_add_u64 v[34:35], v[32:33], 0, v[6:7]
	global_store_dwordx4 v[34:35], v[28:31], off
	s_waitcnt lgkmcnt(1)
	s_nop 0
	v_cvt_pk_bf16_f32 v28, v39, v5
	v_cvt_pk_bf16_f32 v29, v38, v9
	v_cvt_pk_bf16_f32 v30, v37, v11
	s_waitcnt lgkmcnt(0)
	v_cvt_pk_bf16_f32 v31, v36, v40
	ds_read_b32 v5, v27 offset:1124
	ds_read_b32 v7, v27 offset:3180
	ds_read_b32 v11, v27 offset:5236
	ds_read_b32 v36, v27 offset:6264
	ds_read_b32 v37, v27 offset:4208
	ds_read_b32 v38, v27 offset:2152
	ds_read_b32 v39, v27 offset:96
	ds_read_b32 v40, v27 offset:7292
	v_mov_b32_e32 v9, v3
	v_lshl_add_u64 v[34:35], v[32:33], 0, v[8:9]
	global_store_dwordx4 v[34:35], v[28:31], off
	s_waitcnt lgkmcnt(1)
	s_nop 0
	v_cvt_pk_bf16_f32 v28, v39, v5
	v_cvt_pk_bf16_f32 v29, v38, v7
	v_cvt_pk_bf16_f32 v30, v37, v11
	v_mov_b32_e32 v11, v3
	v_lshl_add_u64 v[32:33], v[32:33], 0, v[10:11]
	s_waitcnt lgkmcnt(0)
	v_cvt_pk_bf16_f32 v31, v36, v40
	global_store_dwordx4 v[32:33], v[28:31], off
	s_branch .LBB0_2279
